# accumulator clears dropped: first K-step of each unit peeled with C=0 MFMAs (P1/P3/P6/P7), on top of late restore barrier + early gather ids + hoisted bias loads
# speedup vs baseline: 1.0355x; 1.0127x over previous
.Lp1_first:
	s_add_u32 s70, s64, s66
	s_addc_u32 s71, s65, s67
	s_add_u32 s73, s70, 0x100
	v_add_u32_e32 v184, s87, v175
	v_add_u32_e32 v188, s87, v176
	v_add_u32_e32 v192, s88, v175
	v_add_u32_e32 v196, s88, v176
	v_add_u32_e32 v200, s89, v175
	v_add_u32_e32 v204, s89, v176
	v_add_u32_e32 v208, s90, v175
	v_add_u32_e32 v212, s90, v176
	s_addc_u32 vcc_lo, s71, 0
	ds_read_b128 v[184:187], v184
	ds_read_b128 v[188:191], v188
	ds_read_b128 v[192:195], v192
	ds_read_b128 v[196:199], v196
	ds_read_b128 v[200:203], v200
	ds_read_b128 v[204:207], v204
	ds_read_b128 v[208:211], v208
	ds_read_b128 v[212:215], v212
	s_and_b64 s[70:71], s[68:69], exec
	s_cselect_b32 s71, s47, vcc_lo
	s_cselect_b32 s70, s46, s73
	s_add_u32 s73, s15, s66
	s_addc_u32 vcc_lo, s43, s67
	s_and_b64 s[68:69], s[68:69], exec
	s_cselect_b32 s69, s45, vcc_lo
	s_cselect_b32 s68, s44, s73
	v_lshl_add_u64 v[248:249], v[158:159], 0, s[66:67]
	s_add_i32 m0, s77, 0x8000
	ds_read_b128 v[216:219], v178
	ds_read_b128 v[220:223], v178 offset:2048
	ds_read_b128 v[224:227], v179
	ds_read_b128 v[228:231], v179 offset:2048
	ds_read_b128 v[232:235], v178 offset:4096
	ds_read_b128 v[236:239], v178 offset:6144
	ds_read_b128 v[240:243], v179 offset:4096
	ds_read_b128 v[244:247], v179 offset:6144
	global_load_lds_dwordx4 v[248:249], off
	v_lshl_add_u64 v[248:249], v[156:157], 0, s[66:67]
	s_add_i32 m0, s77, 0xa000
	s_nop 0
	global_load_lds_dwordx4 v[248:249], off
	v_lshl_add_u64 v[248:249], v[154:155], 0, s[66:67]
	s_add_i32 m0, s77, 0xc000
	s_nop 0
	global_load_lds_dwordx4 v[248:249], off
	v_lshl_add_u64 v[248:249], v[152:153], 0, s[66:67]
	s_add_i32 m0, s77, 0xe000
	s_nop 0
	global_load_lds_dwordx4 v[248:249], off
	s_waitcnt vmcnt(8)
	s_waitcnt lgkmcnt(0)
	s_barrier
	s_setprio 1
	s_waitcnt lgkmcnt(0)
	v_mfma_f32_16x16x32_bf16 v[126:129], v[184:187], v[216:219], 0
	v_mfma_f32_16x16x32_bf16 v[122:125], v[192:195], v[216:219], 0
	v_mfma_f32_16x16x32_bf16 v[118:121], v[184:187], v[220:223], 0
	v_mfma_f32_16x16x32_bf16 v[114:117], v[192:195], v[220:223], 0
	v_mfma_f32_16x16x32_bf16 v[110:113], v[184:187], v[232:235], 0
	v_mfma_f32_16x16x32_bf16 v[106:109], v[192:195], v[232:235], 0
	v_mfma_f32_16x16x32_bf16 v[102:105], v[184:187], v[236:239], 0
	v_mfma_f32_16x16x32_bf16 v[98:101], v[192:195], v[236:239], 0
	v_mfma_f32_16x16x32_bf16 v[126:129], v[188:191], v[224:227], v[126:129]
	v_mfma_f32_16x16x32_bf16 v[122:125], v[196:199], v[224:227], v[122:125]
	v_mfma_f32_16x16x32_bf16 v[118:121], v[188:191], v[228:231], v[118:121]
	v_mfma_f32_16x16x32_bf16 v[114:117], v[196:199], v[228:231], v[114:117]
	v_mfma_f32_16x16x32_bf16 v[110:113], v[188:191], v[240:243], v[110:113]
	v_mfma_f32_16x16x32_bf16 v[106:109], v[196:199], v[240:243], v[106:109]
	v_mfma_f32_16x16x32_bf16 v[102:105], v[188:191], v[244:247], v[102:105]
	v_mfma_f32_16x16x32_bf16 v[98:101], v[196:199], v[244:247], v[98:101]
	s_setprio 0
	s_setprio 1
	v_mfma_f32_16x16x32_bf16 v[62:65], v[200:203], v[216:219], 0
	v_mfma_f32_16x16x32_bf16 v[58:61], v[208:211], v[216:219], 0
	v_mfma_f32_16x16x32_bf16 v[54:57], v[200:203], v[220:223], 0
	v_mfma_f32_16x16x32_bf16 v[50:53], v[208:211], v[220:223], 0
	v_mfma_f32_16x16x32_bf16 v[46:49], v[200:203], v[232:235], 0
	v_mfma_f32_16x16x32_bf16 v[42:45], v[208:211], v[232:235], 0
	v_mfma_f32_16x16x32_bf16 v[38:41], v[200:203], v[236:239], 0
	v_mfma_f32_16x16x32_bf16 v[34:37], v[208:211], v[236:239], 0
	v_mfma_f32_16x16x32_bf16 v[62:65], v[204:207], v[224:227], v[62:65]
	v_mfma_f32_16x16x32_bf16 v[58:61], v[212:215], v[224:227], v[58:61]
	v_mfma_f32_16x16x32_bf16 v[54:57], v[204:207], v[228:231], v[54:57]
	v_mfma_f32_16x16x32_bf16 v[50:53], v[212:215], v[228:231], v[50:53]
	v_mfma_f32_16x16x32_bf16 v[46:49], v[204:207], v[240:243], v[46:49]
	v_mfma_f32_16x16x32_bf16 v[42:45], v[212:215], v[240:243], v[42:45]
	v_mfma_f32_16x16x32_bf16 v[38:41], v[204:207], v[244:247], v[38:41]
	v_mfma_f32_16x16x32_bf16 v[34:37], v[212:215], v[244:247], v[34:37]
	s_setprio 0
	s_barrier
	s_add_i32 s73, s87, s76
	v_lshl_add_u64 v[248:249], s[68:69], 0, v[142:143]
	s_mov_b32 m0, s73
	ds_read_b128 v[216:219], v178 offset:16384
	ds_read_b128 v[220:223], v178 offset:18432
	ds_read_b128 v[224:227], v179 offset:16384
	ds_read_b128 v[228:231], v179 offset:18432
	ds_read_b128 v[232:235], v178 offset:20480
	ds_read_b128 v[236:239], v178 offset:22528
	ds_read_b128 v[240:243], v179 offset:20480
	ds_read_b128 v[244:247], v179 offset:22528
	global_load_lds_dwordx4 v[248:249], off
	s_add_i32 m0, s73, 0x2000
	s_add_u32 vcc_lo, s68, 0x80000
	v_lshl_add_u64 v[250:251], s[68:69], 0, v[144:145]
	s_addc_u32 vcc_hi, s69, 0
	s_add_i32 s73, s89, s76
	global_load_lds_dwordx4 v[250:251], off
	v_lshl_add_u64 v[252:253], vcc, 0, v[142:143]
	s_mov_b32 m0, s73
	s_nop 0
	global_load_lds_dwordx4 v[252:253], off
	v_lshl_add_u64 v[252:253], vcc, 0, v[144:145]
	s_add_i32 m0, s73, 0x2000
	s_nop 0
	global_load_lds_dwordx4 v[252:253], off
	s_waitcnt vmcnt(6)
	s_waitcnt lgkmcnt(0)
	s_barrier
	s_setprio 1
	s_waitcnt lgkmcnt(0)
	v_mfma_f32_16x16x32_bf16 v[94:97], v[184:187], v[216:219], 0
	v_mfma_f32_16x16x32_bf16 v[90:93], v[192:195], v[216:219], 0
	v_mfma_f32_16x16x32_bf16 v[86:89], v[184:187], v[220:223], 0
	v_mfma_f32_16x16x32_bf16 v[82:85], v[192:195], v[220:223], 0
	v_mfma_f32_16x16x32_bf16 v[78:81], v[184:187], v[232:235], 0
	v_mfma_f32_16x16x32_bf16 v[74:77], v[192:195], v[232:235], 0
	v_mfma_f32_16x16x32_bf16 v[70:73], v[184:187], v[236:239], 0
	v_mfma_f32_16x16x32_bf16 v[66:69], v[192:195], v[236:239], 0
	v_mfma_f32_16x16x32_bf16 v[94:97], v[188:191], v[224:227], v[94:97]
	v_mfma_f32_16x16x32_bf16 v[90:93], v[196:199], v[224:227], v[90:93]
	v_mfma_f32_16x16x32_bf16 v[86:89], v[188:191], v[228:231], v[86:89]
	v_mfma_f32_16x16x32_bf16 v[82:85], v[196:199], v[228:231], v[82:85]
	v_mfma_f32_16x16x32_bf16 v[78:81], v[188:191], v[240:243], v[78:81]
	v_mfma_f32_16x16x32_bf16 v[74:77], v[196:199], v[240:243], v[74:77]
	v_mfma_f32_16x16x32_bf16 v[70:73], v[188:191], v[244:247], v[70:73]
	v_mfma_f32_16x16x32_bf16 v[66:69], v[196:199], v[244:247], v[66:69]
	s_setprio 0
	s_setprio 1
	v_mfma_f32_16x16x32_bf16 v[30:33], v[200:203], v[216:219], 0
	v_mfma_f32_16x16x32_bf16 v[26:29], v[208:211], v[216:219], 0
	v_mfma_f32_16x16x32_bf16 v[22:25], v[200:203], v[220:223], 0
	v_mfma_f32_16x16x32_bf16 v[18:21], v[208:211], v[220:223], 0
	v_mfma_f32_16x16x32_bf16 v[14:17], v[200:203], v[232:235], 0
	v_mfma_f32_16x16x32_bf16 v[10:13], v[208:211], v[232:235], 0
	v_mfma_f32_16x16x32_bf16 v[6:9], v[200:203], v[236:239], 0
	v_mfma_f32_16x16x32_bf16 v[2:5], v[208:211], v[236:239], 0
	v_mfma_f32_16x16x32_bf16 v[30:33], v[204:207], v[224:227], v[30:33]
	v_mfma_f32_16x16x32_bf16 v[26:29], v[212:215], v[224:227], v[26:29]
	v_mfma_f32_16x16x32_bf16 v[22:25], v[204:207], v[228:231], v[22:25]
	v_mfma_f32_16x16x32_bf16 v[18:21], v[212:215], v[228:231], v[18:21]
	v_mfma_f32_16x16x32_bf16 v[14:17], v[204:207], v[240:243], v[14:17]
	v_mfma_f32_16x16x32_bf16 v[10:13], v[212:215], v[240:243], v[10:13]
	v_mfma_f32_16x16x32_bf16 v[6:9], v[204:207], v[244:247], v[6:9]
	v_mfma_f32_16x16x32_bf16 v[2:5], v[212:215], v[244:247], v[2:5]
	s_setprio 0
	s_barrier
	s_branch .Lp1_blk3

.LBB0_100:
	s_lshl_b32 s15, s14, 19
	s_lshl_b32 s43, s14, 8
	v_or_b32_e32 v2, s15, v172
	s_bitset1_b32 s43, 7
	v_lshlrev_b32_e32 v136, 1, v2
	v_or_b32_e32 v2, s43, v168
	v_lshl_or_b32 v138, v2, 12, v169
	v_or_b32_e32 v2, s15, v173
	s_add_u32 s68, s64, 0x80
	v_lshlrev_b32_e32 v140, 1, v2
	v_or_b32_e32 v2, s43, v170
	s_addc_u32 s69, s65, 0
	v_lshl_or_b32 v150, v2, 12, v171
	v_mov_b32_e32 v131, v147
	v_mov_b32_e32 v133, v147
	v_mov_b32_e32 v135, v147
	s_add_u32 s15, s66, 0x100
	v_mov_b32_e32 v2, 0
	v_mov_b32_e32 v137, v147
	v_mov_b32_e32 v141, v147
	v_mov_b32_e32 v139, v147
	v_mov_b32_e32 v151, v147
	v_lshl_add_u64 v[152:153], s[68:69], 0, v[134:135]
	v_lshl_add_u64 v[154:155], s[68:69], 0, v[132:133]
	v_lshl_add_u64 v[156:157], s[68:69], 0, v[130:131]
	v_lshl_add_u64 v[158:159], s[68:69], 0, v[146:147]
	s_addc_u32 s43, s67, 0
	s_mov_b32 s72, -2
	s_mov_b64 s[66:67], 0
	s_andn2_b64 vcc, exec, s[12:13]
	s_cbranch_vccnz .Lp1_entry
	s_barrier

.LBB0_101:
	s_cmp_eq_u32 s66, 0
	s_cbranch_scc1 .Lp1_first
	s_add_u32 s70, s64, s66
	s_addc_u32 s71, s65, s67
	s_add_u32 s73, s70, 0x100
	v_add_u32_e32 v184, s87, v175
	v_add_u32_e32 v188, s87, v176
	v_add_u32_e32 v192, s88, v175
	v_add_u32_e32 v196, s88, v176
	v_add_u32_e32 v200, s89, v175
	v_add_u32_e32 v204, s89, v176
	v_add_u32_e32 v208, s90, v175
	v_add_u32_e32 v212, s90, v176
	s_addc_u32 vcc_lo, s71, 0
	ds_read_b128 v[184:187], v184
	ds_read_b128 v[188:191], v188
	ds_read_b128 v[192:195], v192
	ds_read_b128 v[196:199], v196
	ds_read_b128 v[200:203], v200
	ds_read_b128 v[204:207], v204
	ds_read_b128 v[208:211], v208
	ds_read_b128 v[212:215], v212
	s_and_b64 s[70:71], s[68:69], exec
	s_cselect_b32 s71, s47, vcc_lo
	s_cselect_b32 s70, s46, s73
	s_add_u32 s73, s15, s66
	s_addc_u32 vcc_lo, s43, s67
	s_and_b64 s[68:69], s[68:69], exec
	s_cselect_b32 s69, s45, vcc_lo
	s_cselect_b32 s68, s44, s73
	v_lshl_add_u64 v[248:249], v[158:159], 0, s[66:67]
	s_add_i32 m0, s77, 0x8000
	ds_read_b128 v[216:219], v178
	ds_read_b128 v[220:223], v178 offset:2048
	ds_read_b128 v[224:227], v179
	ds_read_b128 v[228:231], v179 offset:2048
	ds_read_b128 v[232:235], v178 offset:4096
	ds_read_b128 v[236:239], v178 offset:6144
	ds_read_b128 v[240:243], v179 offset:4096
	ds_read_b128 v[244:247], v179 offset:6144
	global_load_lds_dwordx4 v[248:249], off
	v_lshl_add_u64 v[248:249], v[156:157], 0, s[66:67]
	s_add_i32 m0, s77, 0xa000
	s_nop 0
	global_load_lds_dwordx4 v[248:249], off
	v_lshl_add_u64 v[248:249], v[154:155], 0, s[66:67]
	s_add_i32 m0, s77, 0xc000
	s_nop 0
	global_load_lds_dwordx4 v[248:249], off
	v_lshl_add_u64 v[248:249], v[152:153], 0, s[66:67]
	s_add_i32 m0, s77, 0xe000
	s_nop 0
	global_load_lds_dwordx4 v[248:249], off
	s_waitcnt vmcnt(8)
	s_waitcnt lgkmcnt(0)
	s_barrier
	s_setprio 1
	s_waitcnt lgkmcnt(0)
	v_mfma_f32_16x16x32_bf16 v[126:129], v[184:187], v[216:219], v[126:129]
	v_mfma_f32_16x16x32_bf16 v[122:125], v[192:195], v[216:219], v[122:125]
	v_mfma_f32_16x16x32_bf16 v[118:121], v[184:187], v[220:223], v[118:121]
	v_mfma_f32_16x16x32_bf16 v[114:117], v[192:195], v[220:223], v[114:117]
	v_mfma_f32_16x16x32_bf16 v[110:113], v[184:187], v[232:235], v[110:113]
	v_mfma_f32_16x16x32_bf16 v[106:109], v[192:195], v[232:235], v[106:109]
	v_mfma_f32_16x16x32_bf16 v[102:105], v[184:187], v[236:239], v[102:105]
	v_mfma_f32_16x16x32_bf16 v[98:101], v[192:195], v[236:239], v[98:101]
	v_mfma_f32_16x16x32_bf16 v[126:129], v[188:191], v[224:227], v[126:129]
	v_mfma_f32_16x16x32_bf16 v[122:125], v[196:199], v[224:227], v[122:125]
	v_mfma_f32_16x16x32_bf16 v[118:121], v[188:191], v[228:231], v[118:121]
	v_mfma_f32_16x16x32_bf16 v[114:117], v[196:199], v[228:231], v[114:117]
	v_mfma_f32_16x16x32_bf16 v[110:113], v[188:191], v[240:243], v[110:113]
	v_mfma_f32_16x16x32_bf16 v[106:109], v[196:199], v[240:243], v[106:109]
	v_mfma_f32_16x16x32_bf16 v[102:105], v[188:191], v[244:247], v[102:105]
	v_mfma_f32_16x16x32_bf16 v[98:101], v[196:199], v[244:247], v[98:101]
	s_setprio 0
	s_setprio 1
	v_mfma_f32_16x16x32_bf16 v[62:65], v[200:203], v[216:219], v[62:65]
	v_mfma_f32_16x16x32_bf16 v[58:61], v[208:211], v[216:219], v[58:61]
	v_mfma_f32_16x16x32_bf16 v[54:57], v[200:203], v[220:223], v[54:57]
	v_mfma_f32_16x16x32_bf16 v[50:53], v[208:211], v[220:223], v[50:53]
	v_mfma_f32_16x16x32_bf16 v[46:49], v[200:203], v[232:235], v[46:49]
	v_mfma_f32_16x16x32_bf16 v[42:45], v[208:211], v[232:235], v[42:45]
	v_mfma_f32_16x16x32_bf16 v[38:41], v[200:203], v[236:239], v[38:41]
	v_mfma_f32_16x16x32_bf16 v[34:37], v[208:211], v[236:239], v[34:37]
	v_mfma_f32_16x16x32_bf16 v[62:65], v[204:207], v[224:227], v[62:65]
	v_mfma_f32_16x16x32_bf16 v[58:61], v[212:215], v[224:227], v[58:61]
	v_mfma_f32_16x16x32_bf16 v[54:57], v[204:207], v[228:231], v[54:57]
	v_mfma_f32_16x16x32_bf16 v[50:53], v[212:215], v[228:231], v[50:53]
	v_mfma_f32_16x16x32_bf16 v[46:49], v[204:207], v[240:243], v[46:49]
	v_mfma_f32_16x16x32_bf16 v[42:45], v[212:215], v[240:243], v[42:45]
	v_mfma_f32_16x16x32_bf16 v[38:41], v[204:207], v[244:247], v[38:41]
	v_mfma_f32_16x16x32_bf16 v[34:37], v[212:215], v[244:247], v[34:37]
	s_setprio 0
	s_barrier
	s_add_i32 s73, s87, s76
	v_lshl_add_u64 v[248:249], s[68:69], 0, v[142:143]
	s_mov_b32 m0, s73
	ds_read_b128 v[216:219], v178 offset:16384
	ds_read_b128 v[220:223], v178 offset:18432
	ds_read_b128 v[224:227], v179 offset:16384
	ds_read_b128 v[228:231], v179 offset:18432
	ds_read_b128 v[232:235], v178 offset:20480
	ds_read_b128 v[236:239], v178 offset:22528
	ds_read_b128 v[240:243], v179 offset:20480
	ds_read_b128 v[244:247], v179 offset:22528
	global_load_lds_dwordx4 v[248:249], off
	s_add_i32 m0, s73, 0x2000
	s_add_u32 vcc_lo, s68, 0x80000
	v_lshl_add_u64 v[250:251], s[68:69], 0, v[144:145]
	s_addc_u32 vcc_hi, s69, 0
	s_add_i32 s73, s89, s76
	global_load_lds_dwordx4 v[250:251], off
	v_lshl_add_u64 v[252:253], vcc, 0, v[142:143]
	s_mov_b32 m0, s73
	s_nop 0
	global_load_lds_dwordx4 v[252:253], off
	v_lshl_add_u64 v[252:253], vcc, 0, v[144:145]
	s_add_i32 m0, s73, 0x2000
	s_nop 0
	global_load_lds_dwordx4 v[252:253], off
	s_waitcnt vmcnt(6)
	s_waitcnt lgkmcnt(0)
	s_barrier
	s_setprio 1
	s_waitcnt lgkmcnt(0)
	v_mfma_f32_16x16x32_bf16 v[94:97], v[184:187], v[216:219], v[94:97]
	v_mfma_f32_16x16x32_bf16 v[90:93], v[192:195], v[216:219], v[90:93]
	v_mfma_f32_16x16x32_bf16 v[86:89], v[184:187], v[220:223], v[86:89]
	v_mfma_f32_16x16x32_bf16 v[82:85], v[192:195], v[220:223], v[82:85]
	v_mfma_f32_16x16x32_bf16 v[78:81], v[184:187], v[232:235], v[78:81]
	v_mfma_f32_16x16x32_bf16 v[74:77], v[192:195], v[232:235], v[74:77]
	v_mfma_f32_16x16x32_bf16 v[70:73], v[184:187], v[236:239], v[70:73]
	v_mfma_f32_16x16x32_bf16 v[66:69], v[192:195], v[236:239], v[66:69]
	v_mfma_f32_16x16x32_bf16 v[94:97], v[188:191], v[224:227], v[94:97]
	v_mfma_f32_16x16x32_bf16 v[90:93], v[196:199], v[224:227], v[90:93]
	v_mfma_f32_16x16x32_bf16 v[86:89], v[188:191], v[228:231], v[86:89]
	v_mfma_f32_16x16x32_bf16 v[82:85], v[196:199], v[228:231], v[82:85]
	v_mfma_f32_16x16x32_bf16 v[78:81], v[188:191], v[240:243], v[78:81]
	v_mfma_f32_16x16x32_bf16 v[74:77], v[196:199], v[240:243], v[74:77]
	v_mfma_f32_16x16x32_bf16 v[70:73], v[188:191], v[244:247], v[70:73]
	v_mfma_f32_16x16x32_bf16 v[66:69], v[196:199], v[244:247], v[66:69]
	s_setprio 0
	s_setprio 1
	v_mfma_f32_16x16x32_bf16 v[30:33], v[200:203], v[216:219], v[30:33]
	v_mfma_f32_16x16x32_bf16 v[26:29], v[208:211], v[216:219], v[26:29]
	v_mfma_f32_16x16x32_bf16 v[22:25], v[200:203], v[220:223], v[22:25]
	v_mfma_f32_16x16x32_bf16 v[18:21], v[208:211], v[220:223], v[18:21]
	v_mfma_f32_16x16x32_bf16 v[14:17], v[200:203], v[232:235], v[14:17]
	v_mfma_f32_16x16x32_bf16 v[10:13], v[208:211], v[232:235], v[10:13]
	v_mfma_f32_16x16x32_bf16 v[6:9], v[200:203], v[236:239], v[6:9]
	v_mfma_f32_16x16x32_bf16 v[2:5], v[208:211], v[236:239], v[2:5]
	v_mfma_f32_16x16x32_bf16 v[30:33], v[204:207], v[224:227], v[30:33]
	v_mfma_f32_16x16x32_bf16 v[26:29], v[212:215], v[224:227], v[26:29]
	v_mfma_f32_16x16x32_bf16 v[22:25], v[204:207], v[228:231], v[22:25]
	v_mfma_f32_16x16x32_bf16 v[18:21], v[212:215], v[228:231], v[18:21]
	v_mfma_f32_16x16x32_bf16 v[14:17], v[204:207], v[240:243], v[14:17]
	v_mfma_f32_16x16x32_bf16 v[10:13], v[212:215], v[240:243], v[10:13]
	v_mfma_f32_16x16x32_bf16 v[6:9], v[204:207], v[244:247], v[6:9]
	v_mfma_f32_16x16x32_bf16 v[2:5], v[212:215], v[244:247], v[2:5]
	s_setprio 0
	s_barrier
.Lp1_blk3:
	v_add_u32_e32 v184, s92, v175
	v_add_u32_e32 v188, s92, v176
	v_add_u32_e32 v192, s93, v175
	v_add_u32_e32 v196, s93, v176
	v_add_u32_e32 v200, s94, v175
	v_add_u32_e32 v204, s94, v176
	v_add_u32_e32 v208, s95, v175
	v_add_u32_e32 v212, s95, v176
	ds_read_b128 v[184:187], v184
	ds_read_b128 v[188:191], v188
	ds_read_b128 v[192:195], v192
	ds_read_b128 v[196:199], v196
	ds_read_b128 v[200:203], v200
	ds_read_b128 v[204:207], v204
	ds_read_b128 v[208:211], v208
	ds_read_b128 v[212:215], v212
	s_mov_b32 m0, s77
	v_lshl_add_u64 v[166:167], s[70:71], 0, v[166:167]
	ds_read_b128 v[216:219], v178 offset:32768
	ds_read_b128 v[220:223], v178 offset:34816
	ds_read_b128 v[224:227], v179 offset:32768
	ds_read_b128 v[228:231], v179 offset:34816
	ds_read_b128 v[232:235], v178 offset:36864
	ds_read_b128 v[236:239], v178 offset:38912
	ds_read_b128 v[240:243], v179 offset:36864
	ds_read_b128 v[244:247], v179 offset:38912
	global_load_lds_dwordx4 v[166:167], off
	v_lshl_add_u64 v[164:165], s[70:71], 0, v[164:165]
	s_mov_b32 m0, s78
	v_lshl_add_u64 v[162:163], s[70:71], 0, v[162:163]
	global_load_lds_dwordx4 v[164:165], off
	s_mov_b32 m0, s79
	v_lshl_add_u64 v[160:161], s[70:71], 0, v[160:161]
	global_load_lds_dwordx4 v[162:163], off
	s_mov_b32 m0, s80
	s_nop 0
	global_load_lds_dwordx4 v[160:161], off
	s_waitcnt vmcnt(8)
	s_waitcnt lgkmcnt(0)
	s_barrier
	s_setprio 1
	s_waitcnt lgkmcnt(0)
	v_mfma_f32_16x16x32_bf16 v[126:129], v[184:187], v[216:219], v[126:129]
	v_mfma_f32_16x16x32_bf16 v[122:125], v[192:195], v[216:219], v[122:125]
	v_mfma_f32_16x16x32_bf16 v[118:121], v[184:187], v[220:223], v[118:121]
	v_mfma_f32_16x16x32_bf16 v[114:117], v[192:195], v[220:223], v[114:117]
	v_mfma_f32_16x16x32_bf16 v[110:113], v[184:187], v[232:235], v[110:113]
	v_mfma_f32_16x16x32_bf16 v[106:109], v[192:195], v[232:235], v[106:109]
	v_mfma_f32_16x16x32_bf16 v[102:105], v[184:187], v[236:239], v[102:105]
	v_mfma_f32_16x16x32_bf16 v[98:101], v[192:195], v[236:239], v[98:101]
	v_mfma_f32_16x16x32_bf16 v[126:129], v[188:191], v[224:227], v[126:129]
	v_mfma_f32_16x16x32_bf16 v[122:125], v[196:199], v[224:227], v[122:125]
	v_mfma_f32_16x16x32_bf16 v[118:121], v[188:191], v[228:231], v[118:121]
	v_mfma_f32_16x16x32_bf16 v[114:117], v[196:199], v[228:231], v[114:117]
	v_mfma_f32_16x16x32_bf16 v[110:113], v[188:191], v[240:243], v[110:113]
	v_mfma_f32_16x16x32_bf16 v[106:109], v[196:199], v[240:243], v[106:109]
	v_mfma_f32_16x16x32_bf16 v[102:105], v[188:191], v[244:247], v[102:105]
	v_mfma_f32_16x16x32_bf16 v[98:101], v[196:199], v[244:247], v[98:101]
	s_setprio 0
	s_setprio 1
	v_mfma_f32_16x16x32_bf16 v[62:65], v[200:203], v[216:219], v[62:65]
	v_mfma_f32_16x16x32_bf16 v[58:61], v[208:211], v[216:219], v[58:61]
	v_mfma_f32_16x16x32_bf16 v[54:57], v[200:203], v[220:223], v[54:57]
	v_mfma_f32_16x16x32_bf16 v[50:53], v[208:211], v[220:223], v[50:53]
	v_mfma_f32_16x16x32_bf16 v[46:49], v[200:203], v[232:235], v[46:49]
	v_mfma_f32_16x16x32_bf16 v[42:45], v[208:211], v[232:235], v[42:45]
	v_mfma_f32_16x16x32_bf16 v[38:41], v[200:203], v[236:239], v[38:41]
	v_mfma_f32_16x16x32_bf16 v[34:37], v[208:211], v[236:239], v[34:37]
	v_mfma_f32_16x16x32_bf16 v[62:65], v[204:207], v[224:227], v[62:65]
	v_mfma_f32_16x16x32_bf16 v[58:61], v[212:215], v[224:227], v[58:61]
	v_mfma_f32_16x16x32_bf16 v[54:57], v[204:207], v[228:231], v[54:57]
	v_mfma_f32_16x16x32_bf16 v[50:53], v[212:215], v[228:231], v[50:53]
	v_mfma_f32_16x16x32_bf16 v[46:49], v[204:207], v[240:243], v[46:49]
	v_mfma_f32_16x16x32_bf16 v[42:45], v[212:215], v[240:243], v[42:45]
	v_mfma_f32_16x16x32_bf16 v[38:41], v[204:207], v[244:247], v[38:41]
	v_mfma_f32_16x16x32_bf16 v[34:37], v[212:215], v[244:247], v[34:37]
	s_setprio 0
	s_barrier
	s_add_i32 s70, s92, s76
	v_lshl_add_u64 v[240:241], v[248:249], 0, s[8:9]
	s_mov_b32 m0, s70
	ds_read_b128 v[160:163], v178 offset:49152
	ds_read_b128 v[164:167], v178 offset:51200
	ds_read_b128 v[216:219], v179 offset:49152
	ds_read_b128 v[220:223], v179 offset:51200
	ds_read_b128 v[224:227], v178 offset:53248
	ds_read_b128 v[228:231], v178 offset:55296
	ds_read_b128 v[232:235], v179 offset:53248
	ds_read_b128 v[236:239], v179 offset:55296
	global_load_lds_dwordx4 v[240:241], off
	s_add_i32 m0, s70, 0x2000
	s_add_u32 s68, s68, 0x80080
	v_lshl_add_u64 v[240:241], v[250:251], 0, s[8:9]
	s_addc_u32 s69, s69, 0
	s_add_i32 s70, s94, s76
	global_load_lds_dwordx4 v[240:241], off
	v_lshl_add_u64 v[240:241], s[68:69], 0, v[142:143]
	s_mov_b32 m0, s70
	s_nop 0
	global_load_lds_dwordx4 v[240:241], off
	v_lshl_add_u64 v[240:241], s[68:69], 0, v[144:145]
	s_add_i32 m0, s70, 0x2000
	s_nop 0
	global_load_lds_dwordx4 v[240:241], off
	s_waitcnt vmcnt(6)
	s_waitcnt lgkmcnt(0)
	s_barrier
	s_setprio 1
	s_waitcnt lgkmcnt(0)
	v_mfma_f32_16x16x32_bf16 v[94:97], v[184:187], v[160:163], v[94:97]
	v_mfma_f32_16x16x32_bf16 v[90:93], v[192:195], v[160:163], v[90:93]
	v_mfma_f32_16x16x32_bf16 v[86:89], v[184:187], v[164:167], v[86:89]
	v_mfma_f32_16x16x32_bf16 v[82:85], v[192:195], v[164:167], v[82:85]
	v_mfma_f32_16x16x32_bf16 v[78:81], v[184:187], v[224:227], v[78:81]
	v_mfma_f32_16x16x32_bf16 v[74:77], v[192:195], v[224:227], v[74:77]
	v_mfma_f32_16x16x32_bf16 v[70:73], v[184:187], v[228:231], v[70:73]
	v_mfma_f32_16x16x32_bf16 v[66:69], v[192:195], v[228:231], v[66:69]
	v_mfma_f32_16x16x32_bf16 v[94:97], v[188:191], v[216:219], v[94:97]
	v_mfma_f32_16x16x32_bf16 v[90:93], v[196:199], v[216:219], v[90:93]
	v_mfma_f32_16x16x32_bf16 v[86:89], v[188:191], v[220:223], v[86:89]
	v_mfma_f32_16x16x32_bf16 v[82:85], v[196:199], v[220:223], v[82:85]
	v_mfma_f32_16x16x32_bf16 v[78:81], v[188:191], v[232:235], v[78:81]
	v_mfma_f32_16x16x32_bf16 v[74:77], v[196:199], v[232:235], v[74:77]
	v_mfma_f32_16x16x32_bf16 v[70:73], v[188:191], v[236:239], v[70:73]
	v_mfma_f32_16x16x32_bf16 v[66:69], v[196:199], v[236:239], v[66:69]
	s_setprio 0
	s_setprio 1
	v_mfma_f32_16x16x32_bf16 v[30:33], v[200:203], v[160:163], v[30:33]
	v_mfma_f32_16x16x32_bf16 v[26:29], v[208:211], v[160:163], v[26:29]
	v_mfma_f32_16x16x32_bf16 v[22:25], v[200:203], v[164:167], v[22:25]
	v_mfma_f32_16x16x32_bf16 v[18:21], v[208:211], v[164:167], v[18:21]
	v_mfma_f32_16x16x32_bf16 v[14:17], v[200:203], v[224:227], v[14:17]
	v_mfma_f32_16x16x32_bf16 v[10:13], v[208:211], v[224:227], v[10:13]
	v_mfma_f32_16x16x32_bf16 v[6:9], v[200:203], v[228:231], v[6:9]
	v_mfma_f32_16x16x32_bf16 v[2:5], v[208:211], v[228:231], v[2:5]
	v_mfma_f32_16x16x32_bf16 v[30:33], v[204:207], v[216:219], v[30:33]
	v_mfma_f32_16x16x32_bf16 v[26:29], v[212:215], v[216:219], v[26:29]
	v_mfma_f32_16x16x32_bf16 v[22:25], v[204:207], v[220:223], v[22:25]
	v_mfma_f32_16x16x32_bf16 v[18:21], v[212:215], v[220:223], v[18:21]
	v_mfma_f32_16x16x32_bf16 v[14:17], v[204:207], v[232:235], v[14:17]
	v_mfma_f32_16x16x32_bf16 v[10:13], v[212:215], v[232:235], v[10:13]
	v_mfma_f32_16x16x32_bf16 v[6:9], v[204:207], v[236:239], v[6:9]
	v_mfma_f32_16x16x32_bf16 v[2:5], v[212:215], v[236:239], v[2:5]
	s_setprio 0
	s_barrier
	s_add_i32 s72, s72, 2
	s_add_u32 s66, s66, 0x100
	s_addc_u32 s67, s67, 0
	s_cmp_gt_u32 s72, 29
	s_cbranch_scc1 .LBB0_105

.Lp3_first:
	v_add_u32_e32 v183, s45, v174
	v_add_u32_e32 v188, s45, v175
	s_add_u32 s34, s2, s28
	ds_read_b128 v[184:187], v183
	ds_read_b128 v[188:191], v188
	v_add_u32_e32 v183, s46, v174
	v_add_u32_e32 v196, s46, v175
	s_addc_u32 s35, s3, s29
	ds_read_b128 v[192:195], v183
	ds_read_b128 v[196:199], v196
	v_add_u32_e32 v183, s47, v174
	v_add_u32_e32 v204, s47, v175
	s_add_u32 s77, s34, 0x63000100
	ds_read_b128 v[200:203], v183
	ds_read_b128 v[204:207], v204
	v_add_u32_e32 v183, s64, v174
	v_add_u32_e32 v212, s64, v175
	s_addc_u32 s78, s35, 0
	ds_read_b128 v[208:211], v183
	ds_read_b128 v[212:215], v212
	s_and_b64 s[34:35], s[30:31], exec
	s_cselect_b32 s35, s7, s78
	s_cselect_b32 s34, s6, s77
	s_add_u32 s77, s25, s28
	s_addc_u32 s78, s75, s29
	s_and_b64 s[30:31], s[30:31], exec
	s_cselect_b32 s31, s27, s78
	s_cselect_b32 s30, s26, s77
	v_lshl_add_u64 v[248:249], v[158:159], 0, s[28:29]
	s_add_i32 m0, s39, 0x8000
	ds_read_b128 v[216:219], v177
	ds_read_b128 v[220:223], v177 offset:2048
	ds_read_b128 v[224:227], v178
	ds_read_b128 v[228:231], v178 offset:2048
	ds_read_b128 v[232:235], v177 offset:4096
	ds_read_b128 v[236:239], v177 offset:6144
	ds_read_b128 v[240:243], v178 offset:4096
	ds_read_b128 v[244:247], v178 offset:6144
	global_load_lds_dwordx4 v[248:249], off
	v_lshl_add_u64 v[248:249], v[156:157], 0, s[28:29]
	s_add_i32 m0, s39, 0xa000
	s_nop 0
	global_load_lds_dwordx4 v[248:249], off
	v_lshl_add_u64 v[248:249], v[154:155], 0, s[28:29]
	s_add_i32 m0, s39, 0xc000
	s_nop 0
	global_load_lds_dwordx4 v[248:249], off
	v_lshl_add_u64 v[248:249], v[144:145], 0, s[28:29]
	s_add_i32 m0, s39, 0xe000
	s_nop 0
	global_load_lds_dwordx4 v[248:249], off
	s_waitcnt vmcnt(8)
	s_waitcnt lgkmcnt(0)
	s_barrier
	s_setprio 1
	s_waitcnt lgkmcnt(0)
	v_mfma_f32_16x16x32_bf16 v[126:129], v[184:187], v[216:219], 0
	v_mfma_f32_16x16x32_bf16 v[122:125], v[192:195], v[216:219], 0
	v_mfma_f32_16x16x32_bf16 v[118:121], v[184:187], v[220:223], 0
	v_mfma_f32_16x16x32_bf16 v[114:117], v[192:195], v[220:223], 0
	v_mfma_f32_16x16x32_bf16 v[110:113], v[184:187], v[232:235], 0
	v_mfma_f32_16x16x32_bf16 v[102:105], v[192:195], v[232:235], 0
	v_mfma_f32_16x16x32_bf16 v[94:97], v[184:187], v[236:239], 0
	v_mfma_f32_16x16x32_bf16 v[86:89], v[192:195], v[236:239], 0
	v_mfma_f32_16x16x32_bf16 v[126:129], v[188:191], v[224:227], v[126:129]
	v_mfma_f32_16x16x32_bf16 v[122:125], v[196:199], v[224:227], v[122:125]
	v_mfma_f32_16x16x32_bf16 v[118:121], v[188:191], v[228:231], v[118:121]
	v_mfma_f32_16x16x32_bf16 v[114:117], v[196:199], v[228:231], v[114:117]
	v_mfma_f32_16x16x32_bf16 v[110:113], v[188:191], v[240:243], v[110:113]
	v_mfma_f32_16x16x32_bf16 v[102:105], v[196:199], v[240:243], v[102:105]
	v_mfma_f32_16x16x32_bf16 v[94:97], v[188:191], v[244:247], v[94:97]
	v_mfma_f32_16x16x32_bf16 v[86:89], v[196:199], v[244:247], v[86:89]
	s_setprio 0
	s_setprio 1
	v_mfma_f32_16x16x32_bf16 v[106:109], v[200:203], v[216:219], 0
	v_mfma_f32_16x16x32_bf16 v[98:101], v[208:211], v[216:219], 0
	v_mfma_f32_16x16x32_bf16 v[90:93], v[200:203], v[220:223], 0
	v_mfma_f32_16x16x32_bf16 v[82:85], v[208:211], v[220:223], 0
	v_mfma_f32_16x16x32_bf16 v[78:81], v[200:203], v[232:235], 0
	v_mfma_f32_16x16x32_bf16 v[74:77], v[208:211], v[232:235], 0
	v_mfma_f32_16x16x32_bf16 v[70:73], v[200:203], v[236:239], 0
	v_mfma_f32_16x16x32_bf16 v[66:69], v[208:211], v[236:239], 0
	v_mfma_f32_16x16x32_bf16 v[106:109], v[204:207], v[224:227], v[106:109]
	v_mfma_f32_16x16x32_bf16 v[98:101], v[212:215], v[224:227], v[98:101]
	v_mfma_f32_16x16x32_bf16 v[90:93], v[204:207], v[228:231], v[90:93]
	v_mfma_f32_16x16x32_bf16 v[82:85], v[212:215], v[228:231], v[82:85]
	v_mfma_f32_16x16x32_bf16 v[78:81], v[204:207], v[240:243], v[78:81]
	v_mfma_f32_16x16x32_bf16 v[74:77], v[212:215], v[240:243], v[74:77]
	v_mfma_f32_16x16x32_bf16 v[70:73], v[204:207], v[244:247], v[70:73]
	v_mfma_f32_16x16x32_bf16 v[66:69], v[212:215], v[244:247], v[66:69]
	s_setprio 0
	s_barrier
	s_add_i32 s77, s45, s33
	v_lshl_add_u64 v[248:249], s[30:31], 0, v[146:147]
	s_mov_b32 m0, s77
	ds_read_b128 v[216:219], v177 offset:16384
	ds_read_b128 v[220:223], v177 offset:18432
	ds_read_b128 v[224:227], v178 offset:16384
	ds_read_b128 v[228:231], v178 offset:18432
	ds_read_b128 v[232:235], v177 offset:20480
	ds_read_b128 v[236:239], v177 offset:22528
	ds_read_b128 v[240:243], v178 offset:20480
	ds_read_b128 v[244:247], v178 offset:22528
	global_load_lds_dwordx4 v[248:249], off
	s_add_i32 m0, s77, 0x2000
	s_add_u32 s78, s30, 0x80000
	v_lshl_add_u64 v[250:251], s[30:31], 0, v[148:149]
	s_addc_u32 s79, s31, 0
	s_add_i32 s77, s47, s33
	global_load_lds_dwordx4 v[250:251], off
	v_lshl_add_u64 v[252:253], s[78:79], 0, v[146:147]
	s_mov_b32 m0, s77
	s_nop 0
	global_load_lds_dwordx4 v[252:253], off
	v_lshl_add_u64 v[252:253], s[78:79], 0, v[148:149]
	s_add_i32 m0, s77, 0x2000
	s_nop 0
	global_load_lds_dwordx4 v[252:253], off
	s_waitcnt vmcnt(6)
	s_waitcnt lgkmcnt(0)
	s_barrier
	s_setprio 1
	s_waitcnt lgkmcnt(0)
	v_mfma_f32_16x16x32_bf16 v[62:65], v[184:187], v[216:219], 0
	v_mfma_f32_16x16x32_bf16 v[58:61], v[192:195], v[216:219], 0
	v_mfma_f32_16x16x32_bf16 v[50:53], v[184:187], v[220:223], 0
	v_mfma_f32_16x16x32_bf16 v[42:45], v[192:195], v[220:223], 0
	v_mfma_f32_16x16x32_bf16 v[34:37], v[184:187], v[232:235], 0
	v_mfma_f32_16x16x32_bf16 v[26:29], v[192:195], v[232:235], 0
	v_mfma_f32_16x16x32_bf16 v[18:21], v[184:187], v[236:239], 0
	v_mfma_f32_16x16x32_bf16 v[10:13], v[192:195], v[236:239], 0
	v_mfma_f32_16x16x32_bf16 v[62:65], v[188:191], v[224:227], v[62:65]
	v_mfma_f32_16x16x32_bf16 v[58:61], v[196:199], v[224:227], v[58:61]
	v_mfma_f32_16x16x32_bf16 v[50:53], v[188:191], v[228:231], v[50:53]
	v_mfma_f32_16x16x32_bf16 v[42:45], v[196:199], v[228:231], v[42:45]
	v_mfma_f32_16x16x32_bf16 v[34:37], v[188:191], v[240:243], v[34:37]
	v_mfma_f32_16x16x32_bf16 v[26:29], v[196:199], v[240:243], v[26:29]
	v_mfma_f32_16x16x32_bf16 v[18:21], v[188:191], v[244:247], v[18:21]
	v_mfma_f32_16x16x32_bf16 v[10:13], v[196:199], v[244:247], v[10:13]
	s_setprio 0
	s_setprio 1
	v_mfma_f32_16x16x32_bf16 v[54:57], v[200:203], v[216:219], 0
	v_mfma_f32_16x16x32_bf16 v[46:49], v[208:211], v[216:219], 0
	v_mfma_f32_16x16x32_bf16 v[38:41], v[200:203], v[220:223], 0
	v_mfma_f32_16x16x32_bf16 v[30:33], v[208:211], v[220:223], 0
	v_mfma_f32_16x16x32_bf16 v[22:25], v[200:203], v[232:235], 0
	v_mfma_f32_16x16x32_bf16 v[14:17], v[208:211], v[232:235], 0
	v_mfma_f32_16x16x32_bf16 v[6:9], v[200:203], v[236:239], 0
	v_mfma_f32_16x16x32_bf16 v[2:5], v[208:211], v[236:239], 0
	v_mfma_f32_16x16x32_bf16 v[54:57], v[204:207], v[224:227], v[54:57]
	v_mfma_f32_16x16x32_bf16 v[46:49], v[212:215], v[224:227], v[46:49]
	v_mfma_f32_16x16x32_bf16 v[38:41], v[204:207], v[228:231], v[38:41]
	v_mfma_f32_16x16x32_bf16 v[30:33], v[212:215], v[228:231], v[30:33]
	v_mfma_f32_16x16x32_bf16 v[22:25], v[204:207], v[240:243], v[22:25]
	v_mfma_f32_16x16x32_bf16 v[14:17], v[212:215], v[240:243], v[14:17]
	v_mfma_f32_16x16x32_bf16 v[6:9], v[204:207], v[244:247], v[6:9]
	v_mfma_f32_16x16x32_bf16 v[2:5], v[212:215], v[244:247], v[2:5]
	s_setprio 0
	s_barrier
	s_branch .Lp3_blk3

.LBB0_384:
	s_lshl_b32 s25, s72, 19
	s_lshl_b32 s30, s72, 8
	v_or_b32_e32 v2, s25, v171
	s_bitset1_b32 s30, 7
	v_lshlrev_b32_e32 v136, 1, v2
	v_or_b32_e32 v2, s30, v1
	v_lshl_or_b32 v138, v2, 12, v168
	v_or_b32_e32 v2, s25, v172
	v_lshlrev_b32_e32 v140, 1, v2
	v_or_b32_e32 v2, s30, v169
	v_lshl_or_b32 v142, v2, 12, v170
	v_mov_b32_e32 v131, v151
	v_mov_b32_e32 v133, v151
	v_mov_b32_e32 v135, v151
	s_add_u32 s25, s28, 0x100
	v_mov_b32_e32 v2, 0
	v_mov_b32_e32 v137, v151
	v_mov_b32_e32 v141, v151
	v_mov_b32_e32 v139, v151
	v_mov_b32_e32 v143, v151
	v_lshl_add_u64 v[144:145], s[16:17], 0, v[134:135]
	v_lshl_add_u64 v[154:155], s[16:17], 0, v[132:133]
	v_lshl_add_u64 v[156:157], s[16:17], 0, v[130:131]
	v_lshl_add_u64 v[158:159], s[16:17], 0, v[150:151]
	s_addc_u32 s75, s29, 0
	s_mov_b32 s76, -2
	s_mov_b64 s[28:29], 0
	s_andn2_b64 vcc, exec, s[10:11]
	s_cbranch_vccnz .Lp3_entry
	s_barrier

.LBB0_385:
	s_cmp_eq_u32 s28, 0
	s_cbranch_scc1 .Lp3_first
	v_add_u32_e32 v183, s45, v174
	v_add_u32_e32 v188, s45, v175
	s_add_u32 s34, s2, s28
	ds_read_b128 v[184:187], v183
	ds_read_b128 v[188:191], v188
	v_add_u32_e32 v183, s46, v174
	v_add_u32_e32 v196, s46, v175
	s_addc_u32 s35, s3, s29
	ds_read_b128 v[192:195], v183
	ds_read_b128 v[196:199], v196
	v_add_u32_e32 v183, s47, v174
	v_add_u32_e32 v204, s47, v175
	s_add_u32 s77, s34, 0x63000100
	ds_read_b128 v[200:203], v183
	ds_read_b128 v[204:207], v204
	v_add_u32_e32 v183, s64, v174
	v_add_u32_e32 v212, s64, v175
	s_addc_u32 s78, s35, 0
	ds_read_b128 v[208:211], v183
	ds_read_b128 v[212:215], v212
	s_and_b64 s[34:35], s[30:31], exec
	s_cselect_b32 s35, s7, s78
	s_cselect_b32 s34, s6, s77
	s_add_u32 s77, s25, s28
	s_addc_u32 s78, s75, s29
	s_and_b64 s[30:31], s[30:31], exec
	s_cselect_b32 s31, s27, s78
	s_cselect_b32 s30, s26, s77
	v_lshl_add_u64 v[248:249], v[158:159], 0, s[28:29]
	s_add_i32 m0, s39, 0x8000
	ds_read_b128 v[216:219], v177
	ds_read_b128 v[220:223], v177 offset:2048
	ds_read_b128 v[224:227], v178
	ds_read_b128 v[228:231], v178 offset:2048
	ds_read_b128 v[232:235], v177 offset:4096
	ds_read_b128 v[236:239], v177 offset:6144
	ds_read_b128 v[240:243], v178 offset:4096
	ds_read_b128 v[244:247], v178 offset:6144
	global_load_lds_dwordx4 v[248:249], off
	v_lshl_add_u64 v[248:249], v[156:157], 0, s[28:29]
	s_add_i32 m0, s39, 0xa000
	s_nop 0
	global_load_lds_dwordx4 v[248:249], off
	v_lshl_add_u64 v[248:249], v[154:155], 0, s[28:29]
	s_add_i32 m0, s39, 0xc000
	s_nop 0
	global_load_lds_dwordx4 v[248:249], off
	v_lshl_add_u64 v[248:249], v[144:145], 0, s[28:29]
	s_add_i32 m0, s39, 0xe000
	s_nop 0
	global_load_lds_dwordx4 v[248:249], off
	s_waitcnt vmcnt(8)
	s_waitcnt lgkmcnt(0)
	s_barrier
	s_setprio 1
	s_waitcnt lgkmcnt(0)
	v_mfma_f32_16x16x32_bf16 v[126:129], v[184:187], v[216:219], v[126:129]
	v_mfma_f32_16x16x32_bf16 v[122:125], v[192:195], v[216:219], v[122:125]
	v_mfma_f32_16x16x32_bf16 v[118:121], v[184:187], v[220:223], v[118:121]
	v_mfma_f32_16x16x32_bf16 v[114:117], v[192:195], v[220:223], v[114:117]
	v_mfma_f32_16x16x32_bf16 v[110:113], v[184:187], v[232:235], v[110:113]
	v_mfma_f32_16x16x32_bf16 v[102:105], v[192:195], v[232:235], v[102:105]
	v_mfma_f32_16x16x32_bf16 v[94:97], v[184:187], v[236:239], v[94:97]
	v_mfma_f32_16x16x32_bf16 v[86:89], v[192:195], v[236:239], v[86:89]
	v_mfma_f32_16x16x32_bf16 v[126:129], v[188:191], v[224:227], v[126:129]
	v_mfma_f32_16x16x32_bf16 v[122:125], v[196:199], v[224:227], v[122:125]
	v_mfma_f32_16x16x32_bf16 v[118:121], v[188:191], v[228:231], v[118:121]
	v_mfma_f32_16x16x32_bf16 v[114:117], v[196:199], v[228:231], v[114:117]
	v_mfma_f32_16x16x32_bf16 v[110:113], v[188:191], v[240:243], v[110:113]
	v_mfma_f32_16x16x32_bf16 v[102:105], v[196:199], v[240:243], v[102:105]
	v_mfma_f32_16x16x32_bf16 v[94:97], v[188:191], v[244:247], v[94:97]
	v_mfma_f32_16x16x32_bf16 v[86:89], v[196:199], v[244:247], v[86:89]
	s_setprio 0
	s_setprio 1
	v_mfma_f32_16x16x32_bf16 v[106:109], v[200:203], v[216:219], v[106:109]
	v_mfma_f32_16x16x32_bf16 v[98:101], v[208:211], v[216:219], v[98:101]
	v_mfma_f32_16x16x32_bf16 v[90:93], v[200:203], v[220:223], v[90:93]
	v_mfma_f32_16x16x32_bf16 v[82:85], v[208:211], v[220:223], v[82:85]
	v_mfma_f32_16x16x32_bf16 v[78:81], v[200:203], v[232:235], v[78:81]
	v_mfma_f32_16x16x32_bf16 v[74:77], v[208:211], v[232:235], v[74:77]
	v_mfma_f32_16x16x32_bf16 v[70:73], v[200:203], v[236:239], v[70:73]
	v_mfma_f32_16x16x32_bf16 v[66:69], v[208:211], v[236:239], v[66:69]
	v_mfma_f32_16x16x32_bf16 v[106:109], v[204:207], v[224:227], v[106:109]
	v_mfma_f32_16x16x32_bf16 v[98:101], v[212:215], v[224:227], v[98:101]
	v_mfma_f32_16x16x32_bf16 v[90:93], v[204:207], v[228:231], v[90:93]
	v_mfma_f32_16x16x32_bf16 v[82:85], v[212:215], v[228:231], v[82:85]
	v_mfma_f32_16x16x32_bf16 v[78:81], v[204:207], v[240:243], v[78:81]
	v_mfma_f32_16x16x32_bf16 v[74:77], v[212:215], v[240:243], v[74:77]
	v_mfma_f32_16x16x32_bf16 v[70:73], v[204:207], v[244:247], v[70:73]
	v_mfma_f32_16x16x32_bf16 v[66:69], v[212:215], v[244:247], v[66:69]
	s_setprio 0
	s_barrier
	s_add_i32 s77, s45, s33
	v_lshl_add_u64 v[248:249], s[30:31], 0, v[146:147]
	s_mov_b32 m0, s77
	ds_read_b128 v[216:219], v177 offset:16384
	ds_read_b128 v[220:223], v177 offset:18432
	ds_read_b128 v[224:227], v178 offset:16384
	ds_read_b128 v[228:231], v178 offset:18432
	ds_read_b128 v[232:235], v177 offset:20480
	ds_read_b128 v[236:239], v177 offset:22528
	ds_read_b128 v[240:243], v178 offset:20480
	ds_read_b128 v[244:247], v178 offset:22528
	global_load_lds_dwordx4 v[248:249], off
	s_add_i32 m0, s77, 0x2000
	s_add_u32 s78, s30, 0x80000
	v_lshl_add_u64 v[250:251], s[30:31], 0, v[148:149]
	s_addc_u32 s79, s31, 0
	s_add_i32 s77, s47, s33
	global_load_lds_dwordx4 v[250:251], off
	v_lshl_add_u64 v[252:253], s[78:79], 0, v[146:147]
	s_mov_b32 m0, s77
	s_nop 0
	global_load_lds_dwordx4 v[252:253], off
	v_lshl_add_u64 v[252:253], s[78:79], 0, v[148:149]
	s_add_i32 m0, s77, 0x2000
	s_nop 0
	global_load_lds_dwordx4 v[252:253], off
	s_waitcnt vmcnt(6)
	s_waitcnt lgkmcnt(0)
	s_barrier
	s_setprio 1
	s_waitcnt lgkmcnt(0)
	v_mfma_f32_16x16x32_bf16 v[62:65], v[184:187], v[216:219], v[62:65]
	v_mfma_f32_16x16x32_bf16 v[58:61], v[192:195], v[216:219], v[58:61]
	v_mfma_f32_16x16x32_bf16 v[50:53], v[184:187], v[220:223], v[50:53]
	v_mfma_f32_16x16x32_bf16 v[42:45], v[192:195], v[220:223], v[42:45]
	v_mfma_f32_16x16x32_bf16 v[34:37], v[184:187], v[232:235], v[34:37]
	v_mfma_f32_16x16x32_bf16 v[26:29], v[192:195], v[232:235], v[26:29]
	v_mfma_f32_16x16x32_bf16 v[18:21], v[184:187], v[236:239], v[18:21]
	v_mfma_f32_16x16x32_bf16 v[10:13], v[192:195], v[236:239], v[10:13]
	v_mfma_f32_16x16x32_bf16 v[62:65], v[188:191], v[224:227], v[62:65]
	v_mfma_f32_16x16x32_bf16 v[58:61], v[196:199], v[224:227], v[58:61]
	v_mfma_f32_16x16x32_bf16 v[50:53], v[188:191], v[228:231], v[50:53]
	v_mfma_f32_16x16x32_bf16 v[42:45], v[196:199], v[228:231], v[42:45]
	v_mfma_f32_16x16x32_bf16 v[34:37], v[188:191], v[240:243], v[34:37]
	v_mfma_f32_16x16x32_bf16 v[26:29], v[196:199], v[240:243], v[26:29]
	v_mfma_f32_16x16x32_bf16 v[18:21], v[188:191], v[244:247], v[18:21]
	v_mfma_f32_16x16x32_bf16 v[10:13], v[196:199], v[244:247], v[10:13]
	s_setprio 0
	s_setprio 1
	v_mfma_f32_16x16x32_bf16 v[54:57], v[200:203], v[216:219], v[54:57]
	v_mfma_f32_16x16x32_bf16 v[46:49], v[208:211], v[216:219], v[46:49]
	v_mfma_f32_16x16x32_bf16 v[38:41], v[200:203], v[220:223], v[38:41]
	v_mfma_f32_16x16x32_bf16 v[30:33], v[208:211], v[220:223], v[30:33]
	v_mfma_f32_16x16x32_bf16 v[22:25], v[200:203], v[232:235], v[22:25]
	v_mfma_f32_16x16x32_bf16 v[14:17], v[208:211], v[232:235], v[14:17]
	v_mfma_f32_16x16x32_bf16 v[6:9], v[200:203], v[236:239], v[6:9]
	v_mfma_f32_16x16x32_bf16 v[2:5], v[208:211], v[236:239], v[2:5]
	v_mfma_f32_16x16x32_bf16 v[54:57], v[204:207], v[224:227], v[54:57]
	v_mfma_f32_16x16x32_bf16 v[46:49], v[212:215], v[224:227], v[46:49]
	v_mfma_f32_16x16x32_bf16 v[38:41], v[204:207], v[228:231], v[38:41]
	v_mfma_f32_16x16x32_bf16 v[30:33], v[212:215], v[228:231], v[30:33]
	v_mfma_f32_16x16x32_bf16 v[22:25], v[204:207], v[240:243], v[22:25]
	v_mfma_f32_16x16x32_bf16 v[14:17], v[212:215], v[240:243], v[14:17]
	v_mfma_f32_16x16x32_bf16 v[6:9], v[204:207], v[244:247], v[6:9]
	v_mfma_f32_16x16x32_bf16 v[2:5], v[212:215], v[244:247], v[2:5]
	s_setprio 0
	s_barrier
.Lp3_blk3:
	v_add_u32_e32 v183, s65, v174
	v_add_u32_e32 v188, s65, v175
	ds_read_b128 v[184:187], v183
	ds_read_b128 v[188:191], v188
	v_add_u32_e32 v183, s66, v174
	v_add_u32_e32 v196, s66, v175
	ds_read_b128 v[192:195], v183
	ds_read_b128 v[196:199], v196
	v_add_u32_e32 v183, s67, v174
	v_add_u32_e32 v204, s67, v175
	ds_read_b128 v[200:203], v183
	ds_read_b128 v[204:207], v204
	v_add_u32_e32 v183, s68, v174
	v_add_u32_e32 v212, s68, v175
	ds_read_b128 v[208:211], v183
	ds_read_b128 v[212:215], v212
	s_mov_b32 m0, s39
	v_lshl_add_u64 v[166:167], s[34:35], 0, v[166:167]
	ds_read_b128 v[216:219], v177 offset:32768
	ds_read_b128 v[220:223], v177 offset:34816
	ds_read_b128 v[224:227], v178 offset:32768
	ds_read_b128 v[228:231], v178 offset:34816
	ds_read_b128 v[232:235], v177 offset:36864
	ds_read_b128 v[236:239], v177 offset:38912
	ds_read_b128 v[240:243], v178 offset:36864
	ds_read_b128 v[244:247], v178 offset:38912
	global_load_lds_dwordx4 v[166:167], off
	v_lshl_add_u64 v[164:165], s[34:35], 0, v[164:165]
	s_mov_b32 m0, s40
	v_lshl_add_u64 v[162:163], s[34:35], 0, v[162:163]
	global_load_lds_dwordx4 v[164:165], off
	s_mov_b32 m0, s41
	v_lshl_add_u64 v[160:161], s[34:35], 0, v[160:161]
	global_load_lds_dwordx4 v[162:163], off
	s_mov_b32 m0, s42
	s_nop 0
	global_load_lds_dwordx4 v[160:161], off
	s_waitcnt vmcnt(8)
	s_waitcnt lgkmcnt(0)
	s_barrier
	s_setprio 1
	s_waitcnt lgkmcnt(0)
	v_mfma_f32_16x16x32_bf16 v[126:129], v[184:187], v[216:219], v[126:129]
	v_mfma_f32_16x16x32_bf16 v[122:125], v[192:195], v[216:219], v[122:125]
	v_mfma_f32_16x16x32_bf16 v[118:121], v[184:187], v[220:223], v[118:121]
	v_mfma_f32_16x16x32_bf16 v[114:117], v[192:195], v[220:223], v[114:117]
	v_mfma_f32_16x16x32_bf16 v[110:113], v[184:187], v[232:235], v[110:113]
	v_mfma_f32_16x16x32_bf16 v[102:105], v[192:195], v[232:235], v[102:105]
	v_mfma_f32_16x16x32_bf16 v[94:97], v[184:187], v[236:239], v[94:97]
	v_mfma_f32_16x16x32_bf16 v[86:89], v[192:195], v[236:239], v[86:89]
	v_mfma_f32_16x16x32_bf16 v[126:129], v[188:191], v[224:227], v[126:129]
	v_mfma_f32_16x16x32_bf16 v[122:125], v[196:199], v[224:227], v[122:125]
	v_mfma_f32_16x16x32_bf16 v[118:121], v[188:191], v[228:231], v[118:121]
	v_mfma_f32_16x16x32_bf16 v[114:117], v[196:199], v[228:231], v[114:117]
	v_mfma_f32_16x16x32_bf16 v[110:113], v[188:191], v[240:243], v[110:113]
	v_mfma_f32_16x16x32_bf16 v[102:105], v[196:199], v[240:243], v[102:105]
	v_mfma_f32_16x16x32_bf16 v[94:97], v[188:191], v[244:247], v[94:97]
	v_mfma_f32_16x16x32_bf16 v[86:89], v[196:199], v[244:247], v[86:89]
	s_setprio 0
	s_setprio 1
	v_mfma_f32_16x16x32_bf16 v[106:109], v[200:203], v[216:219], v[106:109]
	v_mfma_f32_16x16x32_bf16 v[98:101], v[208:211], v[216:219], v[98:101]
	v_mfma_f32_16x16x32_bf16 v[90:93], v[200:203], v[220:223], v[90:93]
	v_mfma_f32_16x16x32_bf16 v[82:85], v[208:211], v[220:223], v[82:85]
	v_mfma_f32_16x16x32_bf16 v[78:81], v[200:203], v[232:235], v[78:81]
	v_mfma_f32_16x16x32_bf16 v[74:77], v[208:211], v[232:235], v[74:77]
	v_mfma_f32_16x16x32_bf16 v[70:73], v[200:203], v[236:239], v[70:73]
	v_mfma_f32_16x16x32_bf16 v[66:69], v[208:211], v[236:239], v[66:69]
	v_mfma_f32_16x16x32_bf16 v[106:109], v[204:207], v[224:227], v[106:109]
	v_mfma_f32_16x16x32_bf16 v[98:101], v[212:215], v[224:227], v[98:101]
	v_mfma_f32_16x16x32_bf16 v[90:93], v[204:207], v[228:231], v[90:93]
	v_mfma_f32_16x16x32_bf16 v[82:85], v[212:215], v[228:231], v[82:85]
	v_mfma_f32_16x16x32_bf16 v[78:81], v[204:207], v[240:243], v[78:81]
	v_mfma_f32_16x16x32_bf16 v[74:77], v[212:215], v[240:243], v[74:77]
	v_mfma_f32_16x16x32_bf16 v[70:73], v[204:207], v[244:247], v[70:73]
	v_mfma_f32_16x16x32_bf16 v[66:69], v[212:215], v[244:247], v[66:69]
	s_setprio 0
	s_barrier
	s_add_i32 s34, s65, s33
	v_lshl_add_u64 v[240:241], v[248:249], 0, s[8:9]
	s_mov_b32 m0, s34
	ds_read_b128 v[160:163], v177 offset:49152
	ds_read_b128 v[164:167], v177 offset:51200
	ds_read_b128 v[216:219], v178 offset:49152
	ds_read_b128 v[220:223], v178 offset:51200
	ds_read_b128 v[224:227], v177 offset:53248
	ds_read_b128 v[228:231], v177 offset:55296
	ds_read_b128 v[232:235], v178 offset:53248
	ds_read_b128 v[236:239], v178 offset:55296
	global_load_lds_dwordx4 v[240:241], off
	s_add_i32 m0, s34, 0x2000
	s_add_u32 s30, s30, 0x80080
	v_lshl_add_u64 v[240:241], v[250:251], 0, s[8:9]
	s_addc_u32 s31, s31, 0
	s_add_i32 s34, s67, s33
	global_load_lds_dwordx4 v[240:241], off
	v_lshl_add_u64 v[240:241], s[30:31], 0, v[146:147]
	s_mov_b32 m0, s34
	s_nop 0
	global_load_lds_dwordx4 v[240:241], off
	v_lshl_add_u64 v[240:241], s[30:31], 0, v[148:149]
	s_add_i32 m0, s34, 0x2000
	s_nop 0
	global_load_lds_dwordx4 v[240:241], off
	s_waitcnt vmcnt(6)
	s_waitcnt lgkmcnt(0)
	s_barrier
	s_setprio 1
	s_waitcnt lgkmcnt(0)
	v_mfma_f32_16x16x32_bf16 v[62:65], v[184:187], v[160:163], v[62:65]
	v_mfma_f32_16x16x32_bf16 v[58:61], v[192:195], v[160:163], v[58:61]
	v_mfma_f32_16x16x32_bf16 v[50:53], v[184:187], v[164:167], v[50:53]
	v_mfma_f32_16x16x32_bf16 v[42:45], v[192:195], v[164:167], v[42:45]
	v_mfma_f32_16x16x32_bf16 v[34:37], v[184:187], v[224:227], v[34:37]
	v_mfma_f32_16x16x32_bf16 v[26:29], v[192:195], v[224:227], v[26:29]
	v_mfma_f32_16x16x32_bf16 v[18:21], v[184:187], v[228:231], v[18:21]
	v_mfma_f32_16x16x32_bf16 v[10:13], v[192:195], v[228:231], v[10:13]
	v_mfma_f32_16x16x32_bf16 v[62:65], v[188:191], v[216:219], v[62:65]
	v_mfma_f32_16x16x32_bf16 v[58:61], v[196:199], v[216:219], v[58:61]
	v_mfma_f32_16x16x32_bf16 v[50:53], v[188:191], v[220:223], v[50:53]
	v_mfma_f32_16x16x32_bf16 v[42:45], v[196:199], v[220:223], v[42:45]
	v_mfma_f32_16x16x32_bf16 v[34:37], v[188:191], v[232:235], v[34:37]
	v_mfma_f32_16x16x32_bf16 v[26:29], v[196:199], v[232:235], v[26:29]
	v_mfma_f32_16x16x32_bf16 v[18:21], v[188:191], v[236:239], v[18:21]
	v_mfma_f32_16x16x32_bf16 v[10:13], v[196:199], v[236:239], v[10:13]
	s_setprio 0
	s_setprio 1
	v_mfma_f32_16x16x32_bf16 v[54:57], v[200:203], v[160:163], v[54:57]
	v_mfma_f32_16x16x32_bf16 v[46:49], v[208:211], v[160:163], v[46:49]
	v_mfma_f32_16x16x32_bf16 v[38:41], v[200:203], v[164:167], v[38:41]
	v_mfma_f32_16x16x32_bf16 v[30:33], v[208:211], v[164:167], v[30:33]
	v_mfma_f32_16x16x32_bf16 v[22:25], v[200:203], v[224:227], v[22:25]
	v_mfma_f32_16x16x32_bf16 v[14:17], v[208:211], v[224:227], v[14:17]
	v_mfma_f32_16x16x32_bf16 v[6:9], v[200:203], v[228:231], v[6:9]
	v_mfma_f32_16x16x32_bf16 v[2:5], v[208:211], v[228:231], v[2:5]
	v_mfma_f32_16x16x32_bf16 v[54:57], v[204:207], v[216:219], v[54:57]
	v_mfma_f32_16x16x32_bf16 v[46:49], v[212:215], v[216:219], v[46:49]
	v_mfma_f32_16x16x32_bf16 v[38:41], v[204:207], v[220:223], v[38:41]
	v_mfma_f32_16x16x32_bf16 v[30:33], v[212:215], v[220:223], v[30:33]
	v_mfma_f32_16x16x32_bf16 v[22:25], v[204:207], v[232:235], v[22:25]
	v_mfma_f32_16x16x32_bf16 v[14:17], v[212:215], v[232:235], v[14:17]
	v_mfma_f32_16x16x32_bf16 v[6:9], v[204:207], v[236:239], v[6:9]
	v_mfma_f32_16x16x32_bf16 v[2:5], v[212:215], v[236:239], v[2:5]
	s_setprio 0
	s_barrier
	s_add_i32 s76, s76, 2
	s_add_u32 s28, s28, 0x100
	s_addc_u32 s29, s29, 0
	s_cmp_gt_u32 s76, 29
	s_cbranch_scc1 .LBB0_389

.Lp6_first:
	s_add_u32 s44, s2, s40
	v_add_u32_e32 v2, s68, v208
	s_addc_u32 s45, s3, s41
	v_add_u32_e32 v3, s68, v209
	ds_read_b128 v[18:21], v2
	ds_read_b128 v[22:25], v3
	v_add_u32_e32 v2, s69, v208
	s_add_u32 s84, s44, 0x56800100
	v_add_u32_e32 v3, s69, v209
	ds_read_b128 v[26:29], v2
	ds_read_b128 v[30:33], v3
	v_add_u32_e32 v2, s70, v208
	v_add_u32_e32 v6, s70, v209
	v_add_u32_e32 v10, s71, v208
	v_add_u32_e32 v14, s71, v209
	s_addc_u32 s85, s45, 0
	ds_read_b128 v[2:5], v2
	ds_read_b128 v[6:9], v6
	ds_read_b128 v[10:13], v10
	ds_read_b128 v[14:17], v14
	s_and_b64 s[44:45], s[42:43], exec
	s_cselect_b32 s45, s9, s85
	s_cselect_b32 s44, s8, s84
	s_add_u32 s84, s29, s40
	s_addc_u32 s85, s37, s41
	s_and_b64 s[42:43], s[42:43], exec
	s_cselect_b32 s43, s31, s85
	s_cselect_b32 s42, s30, s84
	v_lshl_add_u64 v[200:201], v[190:191], 0, s[40:41]
	s_add_i32 m0, s35, 0x8000
	ds_read_b128 v[218:221], v211
	ds_read_b128 v[226:229], v211 offset:2048
	ds_read_b128 v[222:225], v212
	ds_read_b128 v[230:233], v212 offset:2048
	ds_read_b128 v[234:237], v211 offset:4096
	ds_read_b128 v[242:245], v211 offset:6144
	ds_read_b128 v[238:241], v212 offset:4096
	ds_read_b128 v[246:249], v212 offset:6144
	global_load_lds_dwordx4 v[200:201], off
	v_lshl_add_u64 v[200:201], v[188:189], 0, s[40:41]
	s_add_i32 m0, s35, 0xa000
	s_nop 0
	global_load_lds_dwordx4 v[200:201], off
	v_lshl_add_u64 v[200:201], v[186:187], 0, s[40:41]
	s_add_i32 m0, s35, 0xc000
	s_nop 0
	global_load_lds_dwordx4 v[200:201], off
	v_lshl_add_u64 v[200:201], v[184:185], 0, s[40:41]
	s_add_i32 m0, s35, 0xe000
	s_nop 0
	global_load_lds_dwordx4 v[200:201], off
	s_waitcnt vmcnt(8)
	s_waitcnt lgkmcnt(0)
	s_barrier
	s_setprio 1
	s_waitcnt lgkmcnt(0)
	v_mfma_f32_16x16x128_f8f6f4 v[158:161], v[18:25], v[218:225], 0
	v_mfma_f32_16x16x128_f8f6f4 v[154:157], v[26:33], v[218:225], 0
	v_mfma_f32_16x16x128_f8f6f4 v[150:153], v[18:25], v[226:233], 0
	v_mfma_f32_16x16x128_f8f6f4 v[146:149], v[26:33], v[226:233], 0
	v_mfma_f32_16x16x128_f8f6f4 v[126:129], v[18:25], v[234:241], 0
	v_mfma_f32_16x16x128_f8f6f4 v[122:125], v[26:33], v[234:241], 0
	v_mfma_f32_16x16x128_f8f6f4 v[110:113], v[18:25], v[242:249], 0
	v_mfma_f32_16x16x128_f8f6f4 v[106:109], v[26:33], v[242:249], 0
	s_setprio 0
	s_setprio 1
	v_mfma_f32_16x16x128_f8f6f4 v[142:145], v[2:9], v[218:225], 0
	v_mfma_f32_16x16x128_f8f6f4 v[138:141], v[10:17], v[218:225], 0
	v_mfma_f32_16x16x128_f8f6f4 v[134:137], v[2:9], v[226:233], 0
	v_mfma_f32_16x16x128_f8f6f4 v[130:133], v[10:17], v[226:233], 0
	v_mfma_f32_16x16x128_f8f6f4 v[118:121], v[2:9], v[234:241], 0
	v_mfma_f32_16x16x128_f8f6f4 v[114:117], v[10:17], v[234:241], 0
	v_mfma_f32_16x16x128_f8f6f4 v[102:105], v[2:9], v[242:249], 0
	v_mfma_f32_16x16x128_f8f6f4 v[98:101], v[10:17], v[242:249], 0
	s_setprio 0
	s_barrier
	s_add_i32 s84, s68, s33
	v_lshl_add_u64 v[200:201], s[42:43], 0, v[164:165]
	s_mov_b32 m0, s84
	ds_read_b128 v[218:221], v211 offset:16384
	ds_read_b128 v[226:229], v211 offset:18432
	ds_read_b128 v[222:225], v212 offset:16384
	ds_read_b128 v[230:233], v212 offset:18432
	ds_read_b128 v[234:237], v211 offset:20480
	ds_read_b128 v[242:245], v211 offset:22528
	ds_read_b128 v[238:241], v212 offset:20480
	ds_read_b128 v[246:249], v212 offset:22528
	global_load_lds_dwordx4 v[200:201], off
	s_add_i32 m0, s84, 0x2000
	s_add_u32 s84, s42, 0x40000
	v_lshl_add_u64 v[202:203], s[42:43], 0, v[166:167]
	s_addc_u32 s85, s43, 0
	s_add_i32 s86, s70, s33
	global_load_lds_dwordx4 v[202:203], off
	v_lshl_add_u64 v[250:251], s[84:85], 0, v[164:165]
	s_mov_b32 m0, s86
	s_nop 0
	global_load_lds_dwordx4 v[250:251], off
	v_lshl_add_u64 v[250:251], s[84:85], 0, v[166:167]
	s_add_i32 m0, s86, 0x2000
	s_nop 0
	global_load_lds_dwordx4 v[250:251], off
	s_waitcnt vmcnt(6)
	s_waitcnt lgkmcnt(0)
	s_barrier
	s_setprio 1
	s_waitcnt lgkmcnt(0)
	v_mfma_f32_16x16x128_f8f6f4 v[94:97], v[18:25], v[218:225], 0
	v_mfma_f32_16x16x128_f8f6f4 v[90:93], v[26:33], v[218:225], 0
	v_mfma_f32_16x16x128_f8f6f4 v[78:81], v[18:25], v[226:233], 0
	v_mfma_f32_16x16x128_f8f6f4 v[74:77], v[26:33], v[226:233], 0
	v_mfma_f32_16x16x128_f8f6f4 v[62:65], v[18:25], v[234:241], 0
	v_mfma_f32_16x16x128_f8f6f4 v[58:61], v[26:33], v[234:241], 0
	v_mfma_f32_16x16x128_f8f6f4 v[46:49], v[18:25], v[242:249], 0
	v_mfma_f32_16x16x128_f8f6f4 v[42:45], v[26:33], v[242:249], 0
	s_setprio 0
	s_setprio 1
	v_mfma_f32_16x16x128_f8f6f4 v[86:89], v[2:9], v[218:225], 0
	v_mfma_f32_16x16x128_f8f6f4 v[82:85], v[10:17], v[218:225], 0
	v_mfma_f32_16x16x128_f8f6f4 v[70:73], v[2:9], v[226:233], 0
	v_mfma_f32_16x16x128_f8f6f4 v[66:69], v[10:17], v[226:233], 0
	v_mfma_f32_16x16x128_f8f6f4 v[54:57], v[2:9], v[234:241], 0
	v_mfma_f32_16x16x128_f8f6f4 v[50:53], v[10:17], v[234:241], 0
	v_mfma_f32_16x16x128_f8f6f4 v[38:41], v[2:9], v[242:249], 0
	v_mfma_f32_16x16x128_f8f6f4 v[34:37], v[10:17], v[242:249], 0
	s_setprio 0
	s_barrier
	s_branch .Lp6_blk3

.LBB0_776:
	s_lshl_b32 s27, s81, 8
	v_or_b32_e32 v214, s27, v1
	v_or_b32_e32 v216, s27, v204
	s_lshl_b32 s27, s28, 2
	s_add_i32 s27, s27, 0
	s_lshl_b64 s[38:39], s[28:29], 16
	s_add_i32 s27, s27, 0x22100
	s_add_u32 s38, s50, s38
	s_addc_u32 s39, s51, s39
	v_mov_b32_e32 v177, v163
	v_mov_b32_e32 v179, v163
	v_mov_b32_e32 v181, v163
	v_mov_b32_e32 v183, v163
	s_add_u32 s29, s40, 0x100
	v_mov_b32_e32 v34, 0
	v_or_b32_e32 v215, 0x80, v214
	v_or_b32_e32 v217, 0x80, v216
	v_lshl_add_u64 v[184:185], s[18:19], 0, v[182:183]
	v_lshl_add_u64 v[186:187], s[18:19], 0, v[180:181]
	v_lshl_add_u64 v[188:189], s[18:19], 0, v[178:179]
	v_lshl_add_u64 v[190:191], s[18:19], 0, v[176:177]
	s_addc_u32 s37, s41, 0
	s_mov_b32 s83, -2
	s_mov_b64 s[40:41], 0
	s_andn2_b64 vcc, exec, s[12:13]
	s_cbranch_vccnz .Lp6_entry
	s_barrier

.LBB0_777:
	s_cmp_eq_u32 s40, 0
	s_cbranch_scc1 .Lp6_first
	s_add_u32 s44, s2, s40
	v_add_u32_e32 v2, s68, v208
	s_addc_u32 s45, s3, s41
	v_add_u32_e32 v3, s68, v209
	ds_read_b128 v[18:21], v2
	ds_read_b128 v[22:25], v3
	v_add_u32_e32 v2, s69, v208
	s_add_u32 s84, s44, 0x56800100
	v_add_u32_e32 v3, s69, v209
	ds_read_b128 v[26:29], v2
	ds_read_b128 v[30:33], v3
	v_add_u32_e32 v2, s70, v208
	v_add_u32_e32 v6, s70, v209
	v_add_u32_e32 v10, s71, v208
	v_add_u32_e32 v14, s71, v209
	s_addc_u32 s85, s45, 0
	ds_read_b128 v[2:5], v2
	ds_read_b128 v[6:9], v6
	ds_read_b128 v[10:13], v10
	ds_read_b128 v[14:17], v14
	s_and_b64 s[44:45], s[42:43], exec
	s_cselect_b32 s45, s9, s85
	s_cselect_b32 s44, s8, s84
	s_add_u32 s84, s29, s40
	s_addc_u32 s85, s37, s41
	s_and_b64 s[42:43], s[42:43], exec
	s_cselect_b32 s43, s31, s85
	s_cselect_b32 s42, s30, s84
	v_lshl_add_u64 v[200:201], v[190:191], 0, s[40:41]
	s_add_i32 m0, s35, 0x8000
	ds_read_b128 v[218:221], v211
	ds_read_b128 v[226:229], v211 offset:2048
	ds_read_b128 v[222:225], v212
	ds_read_b128 v[230:233], v212 offset:2048
	ds_read_b128 v[234:237], v211 offset:4096
	ds_read_b128 v[242:245], v211 offset:6144
	ds_read_b128 v[238:241], v212 offset:4096
	ds_read_b128 v[246:249], v212 offset:6144
	global_load_lds_dwordx4 v[200:201], off
	v_lshl_add_u64 v[200:201], v[188:189], 0, s[40:41]
	s_add_i32 m0, s35, 0xa000
	s_nop 0
	global_load_lds_dwordx4 v[200:201], off
	v_lshl_add_u64 v[200:201], v[186:187], 0, s[40:41]
	s_add_i32 m0, s35, 0xc000
	s_nop 0
	global_load_lds_dwordx4 v[200:201], off
	v_lshl_add_u64 v[200:201], v[184:185], 0, s[40:41]
	s_add_i32 m0, s35, 0xe000
	s_nop 0
	global_load_lds_dwordx4 v[200:201], off
	s_waitcnt vmcnt(8)
	s_waitcnt lgkmcnt(0)
	s_barrier
	s_setprio 1
	s_waitcnt lgkmcnt(0)
	v_mfma_f32_16x16x128_f8f6f4 v[158:161], v[18:25], v[218:225], v[158:161]
	v_mfma_f32_16x16x128_f8f6f4 v[154:157], v[26:33], v[218:225], v[154:157]
	v_mfma_f32_16x16x128_f8f6f4 v[150:153], v[18:25], v[226:233], v[150:153]
	v_mfma_f32_16x16x128_f8f6f4 v[146:149], v[26:33], v[226:233], v[146:149]
	v_mfma_f32_16x16x128_f8f6f4 v[126:129], v[18:25], v[234:241], v[126:129]
	v_mfma_f32_16x16x128_f8f6f4 v[122:125], v[26:33], v[234:241], v[122:125]
	v_mfma_f32_16x16x128_f8f6f4 v[110:113], v[18:25], v[242:249], v[110:113]
	v_mfma_f32_16x16x128_f8f6f4 v[106:109], v[26:33], v[242:249], v[106:109]
	s_setprio 0
	s_setprio 1
	v_mfma_f32_16x16x128_f8f6f4 v[142:145], v[2:9], v[218:225], v[142:145]
	v_mfma_f32_16x16x128_f8f6f4 v[138:141], v[10:17], v[218:225], v[138:141]
	v_mfma_f32_16x16x128_f8f6f4 v[134:137], v[2:9], v[226:233], v[134:137]
	v_mfma_f32_16x16x128_f8f6f4 v[130:133], v[10:17], v[226:233], v[130:133]
	v_mfma_f32_16x16x128_f8f6f4 v[118:121], v[2:9], v[234:241], v[118:121]
	v_mfma_f32_16x16x128_f8f6f4 v[114:117], v[10:17], v[234:241], v[114:117]
	v_mfma_f32_16x16x128_f8f6f4 v[102:105], v[2:9], v[242:249], v[102:105]
	v_mfma_f32_16x16x128_f8f6f4 v[98:101], v[10:17], v[242:249], v[98:101]
	s_setprio 0
	s_barrier
	s_add_i32 s84, s68, s33
	v_lshl_add_u64 v[200:201], s[42:43], 0, v[164:165]
	s_mov_b32 m0, s84
	ds_read_b128 v[218:221], v211 offset:16384
	ds_read_b128 v[226:229], v211 offset:18432
	ds_read_b128 v[222:225], v212 offset:16384
	ds_read_b128 v[230:233], v212 offset:18432
	ds_read_b128 v[234:237], v211 offset:20480
	ds_read_b128 v[242:245], v211 offset:22528
	ds_read_b128 v[238:241], v212 offset:20480
	ds_read_b128 v[246:249], v212 offset:22528
	global_load_lds_dwordx4 v[200:201], off
	s_add_i32 m0, s84, 0x2000
	s_add_u32 s84, s42, 0x40000
	v_lshl_add_u64 v[202:203], s[42:43], 0, v[166:167]
	s_addc_u32 s85, s43, 0
	s_add_i32 s86, s70, s33
	global_load_lds_dwordx4 v[202:203], off
	v_lshl_add_u64 v[250:251], s[84:85], 0, v[164:165]
	s_mov_b32 m0, s86
	s_nop 0
	global_load_lds_dwordx4 v[250:251], off
	v_lshl_add_u64 v[250:251], s[84:85], 0, v[166:167]
	s_add_i32 m0, s86, 0x2000
	s_nop 0
	global_load_lds_dwordx4 v[250:251], off
	s_waitcnt vmcnt(6)
	s_waitcnt lgkmcnt(0)
	s_barrier
	s_setprio 1
	s_waitcnt lgkmcnt(0)
	v_mfma_f32_16x16x128_f8f6f4 v[94:97], v[18:25], v[218:225], v[94:97]
	v_mfma_f32_16x16x128_f8f6f4 v[90:93], v[26:33], v[218:225], v[90:93]
	v_mfma_f32_16x16x128_f8f6f4 v[78:81], v[18:25], v[226:233], v[78:81]
	v_mfma_f32_16x16x128_f8f6f4 v[74:77], v[26:33], v[226:233], v[74:77]
	v_mfma_f32_16x16x128_f8f6f4 v[62:65], v[18:25], v[234:241], v[62:65]
	v_mfma_f32_16x16x128_f8f6f4 v[58:61], v[26:33], v[234:241], v[58:61]
	v_mfma_f32_16x16x128_f8f6f4 v[46:49], v[18:25], v[242:249], v[46:49]
	v_mfma_f32_16x16x128_f8f6f4 v[42:45], v[26:33], v[242:249], v[42:45]
	s_setprio 0
	s_setprio 1
	v_mfma_f32_16x16x128_f8f6f4 v[86:89], v[2:9], v[218:225], v[86:89]
	v_mfma_f32_16x16x128_f8f6f4 v[82:85], v[10:17], v[218:225], v[82:85]
	v_mfma_f32_16x16x128_f8f6f4 v[70:73], v[2:9], v[226:233], v[70:73]
	v_mfma_f32_16x16x128_f8f6f4 v[66:69], v[10:17], v[226:233], v[66:69]
	v_mfma_f32_16x16x128_f8f6f4 v[54:57], v[2:9], v[234:241], v[54:57]
	v_mfma_f32_16x16x128_f8f6f4 v[50:53], v[10:17], v[234:241], v[50:53]
	v_mfma_f32_16x16x128_f8f6f4 v[38:41], v[2:9], v[242:249], v[38:41]
	v_mfma_f32_16x16x128_f8f6f4 v[34:37], v[10:17], v[242:249], v[34:37]
	s_setprio 0
	s_barrier
.Lp6_blk3:
	v_add_u32_e32 v2, s72, v208
	v_add_u32_e32 v6, s72, v209
	v_add_u32_e32 v10, s73, v208
	v_add_u32_e32 v14, s73, v209
	v_add_u32_e32 v18, s74, v208
	v_add_u32_e32 v22, s74, v209
	v_add_u32_e32 v26, s75, v208
	v_add_u32_e32 v30, s75, v209
	ds_read_b128 v[2:5], v2
	ds_read_b128 v[6:9], v6
	ds_read_b128 v[10:13], v10
	ds_read_b128 v[14:17], v14
	ds_read_b128 v[18:21], v18
	ds_read_b128 v[22:25], v22
	ds_read_b128 v[26:29], v26
	ds_read_b128 v[30:33], v30
	s_mov_b32 m0, s35
	v_lshl_add_u64 v[198:199], s[44:45], 0, v[198:199]
	ds_read_b128 v[218:221], v211 offset:32768
	ds_read_b128 v[226:229], v211 offset:34816
	ds_read_b128 v[222:225], v212 offset:32768
	ds_read_b128 v[230:233], v212 offset:34816
	ds_read_b128 v[234:237], v211 offset:36864
	ds_read_b128 v[242:245], v211 offset:38912
	ds_read_b128 v[238:241], v212 offset:36864
	ds_read_b128 v[246:249], v212 offset:38912
	global_load_lds_dwordx4 v[198:199], off
	v_lshl_add_u64 v[196:197], s[44:45], 0, v[196:197]
	s_mov_b32 m0, s55
	v_lshl_add_u64 v[194:195], s[44:45], 0, v[194:195]
	global_load_lds_dwordx4 v[196:197], off
	s_mov_b32 m0, s64
	v_lshl_add_u64 v[192:193], s[44:45], 0, v[192:193]
	global_load_lds_dwordx4 v[194:195], off
	s_mov_b32 m0, s65
	s_nop 0
	global_load_lds_dwordx4 v[192:193], off
	s_waitcnt vmcnt(8)
	s_waitcnt lgkmcnt(0)
	s_barrier
	s_setprio 1
	s_waitcnt lgkmcnt(0)
	v_mfma_f32_16x16x128_f8f6f4 v[158:161], v[2:9], v[218:225], v[158:161]
	v_mfma_f32_16x16x128_f8f6f4 v[154:157], v[10:17], v[218:225], v[154:157]
	v_mfma_f32_16x16x128_f8f6f4 v[150:153], v[2:9], v[226:233], v[150:153]
	v_mfma_f32_16x16x128_f8f6f4 v[146:149], v[10:17], v[226:233], v[146:149]
	v_mfma_f32_16x16x128_f8f6f4 v[126:129], v[2:9], v[234:241], v[126:129]
	v_mfma_f32_16x16x128_f8f6f4 v[122:125], v[10:17], v[234:241], v[122:125]
	v_mfma_f32_16x16x128_f8f6f4 v[110:113], v[2:9], v[242:249], v[110:113]
	v_mfma_f32_16x16x128_f8f6f4 v[106:109], v[10:17], v[242:249], v[106:109]
	s_setprio 0
	s_setprio 1
	v_mfma_f32_16x16x128_f8f6f4 v[142:145], v[18:25], v[218:225], v[142:145]
	v_mfma_f32_16x16x128_f8f6f4 v[138:141], v[26:33], v[218:225], v[138:141]
	v_mfma_f32_16x16x128_f8f6f4 v[134:137], v[18:25], v[226:233], v[134:137]
	v_mfma_f32_16x16x128_f8f6f4 v[130:133], v[26:33], v[226:233], v[130:133]
	v_mfma_f32_16x16x128_f8f6f4 v[118:121], v[18:25], v[234:241], v[118:121]
	v_mfma_f32_16x16x128_f8f6f4 v[114:117], v[26:33], v[234:241], v[114:117]
	v_mfma_f32_16x16x128_f8f6f4 v[102:105], v[18:25], v[242:249], v[102:105]
	v_mfma_f32_16x16x128_f8f6f4 v[98:101], v[26:33], v[242:249], v[98:101]
	s_setprio 0
	s_barrier
	s_add_i32 s44, s72, s33
	v_lshl_add_u64 v[200:201], v[200:201], 0, s[10:11]
	s_mov_b32 m0, s44
	ds_read_b128 v[192:195], v211 offset:49152
	ds_read_b128 v[218:221], v211 offset:51200
	ds_read_b128 v[196:199], v212 offset:49152
	ds_read_b128 v[222:225], v212 offset:51200
	ds_read_b128 v[226:229], v211 offset:53248
	ds_read_b128 v[234:237], v211 offset:55296
	ds_read_b128 v[230:233], v212 offset:53248
	ds_read_b128 v[238:241], v212 offset:55296
	global_load_lds_dwordx4 v[200:201], off
	s_add_i32 m0, s44, 0x2000
	s_add_u32 s42, s42, 0x40080
	v_lshl_add_u64 v[200:201], v[202:203], 0, s[10:11]
	s_addc_u32 s43, s43, 0
	s_add_i32 s44, s74, s33
	global_load_lds_dwordx4 v[200:201], off
	v_lshl_add_u64 v[200:201], s[42:43], 0, v[164:165]
	s_mov_b32 m0, s44
	s_nop 0
	global_load_lds_dwordx4 v[200:201], off
	v_lshl_add_u64 v[200:201], s[42:43], 0, v[166:167]
	s_add_i32 m0, s44, 0x2000
	s_nop 0
	global_load_lds_dwordx4 v[200:201], off
	s_waitcnt vmcnt(6)
	s_waitcnt lgkmcnt(0)
	s_barrier
	s_setprio 1
	s_waitcnt lgkmcnt(0)
	v_mfma_f32_16x16x128_f8f6f4 v[94:97], v[2:9], v[192:199], v[94:97]
	v_mfma_f32_16x16x128_f8f6f4 v[90:93], v[10:17], v[192:199], v[90:93]
	v_mfma_f32_16x16x128_f8f6f4 v[78:81], v[2:9], v[218:225], v[78:81]
	v_mfma_f32_16x16x128_f8f6f4 v[74:77], v[10:17], v[218:225], v[74:77]
	v_mfma_f32_16x16x128_f8f6f4 v[62:65], v[2:9], v[226:233], v[62:65]
	v_mfma_f32_16x16x128_f8f6f4 v[58:61], v[10:17], v[226:233], v[58:61]
	v_mfma_f32_16x16x128_f8f6f4 v[46:49], v[2:9], v[234:241], v[46:49]
	v_mfma_f32_16x16x128_f8f6f4 v[42:45], v[10:17], v[234:241], v[42:45]
	s_setprio 0
	s_setprio 1
	v_mfma_f32_16x16x128_f8f6f4 v[86:89], v[18:25], v[192:199], v[86:89]
	v_mfma_f32_16x16x128_f8f6f4 v[82:85], v[26:33], v[192:199], v[82:85]
	v_mfma_f32_16x16x128_f8f6f4 v[70:73], v[18:25], v[218:225], v[70:73]
	v_mfma_f32_16x16x128_f8f6f4 v[66:69], v[26:33], v[218:225], v[66:69]
	v_mfma_f32_16x16x128_f8f6f4 v[54:57], v[18:25], v[226:233], v[54:57]
	v_mfma_f32_16x16x128_f8f6f4 v[50:53], v[26:33], v[226:233], v[50:53]
	v_mfma_f32_16x16x128_f8f6f4 v[38:41], v[18:25], v[234:241], v[38:41]
	v_mfma_f32_16x16x128_f8f6f4 v[34:37], v[26:33], v[234:241], v[34:37]
	s_setprio 0
	s_barrier
	s_add_i32 s83, s83, 2
	s_add_u32 s40, s40, 0x100
	s_addc_u32 s41, s41, 0
	s_cmp_gt_u32 s83, 13
	s_cbranch_scc1 .LBB0_781

.Lp7_first:
	s_add_u32 s48, s2, s44
	v_add_u32_e32 v2, s66, v210
	s_addc_u32 s49, s3, s45
	v_add_u32_e32 v3, s66, v211
	ds_read_b128 v[18:21], v2
	ds_read_b128 v[22:25], v3
	v_add_u32_e32 v2, s67, v210
	s_add_u32 s81, s48, 0x3e800100
	v_add_u32_e32 v3, s67, v211
	ds_read_b128 v[26:29], v2
	ds_read_b128 v[30:33], v3
	v_add_u32_e32 v2, s68, v210
	v_add_u32_e32 v6, s68, v211
	v_add_u32_e32 v10, s69, v210
	v_add_u32_e32 v14, s69, v211
	s_addc_u32 s82, s49, 0
	ds_read_b128 v[2:5], v2
	ds_read_b128 v[6:9], v6
	ds_read_b128 v[10:13], v10
	ds_read_b128 v[14:17], v14
	s_and_b64 s[48:49], s[46:47], exec
	s_cselect_b32 s49, s9, s82
	s_cselect_b32 s48, s8, s81
	s_add_u32 s81, s35, s44
	s_addc_u32 s82, s37, s45
	s_and_b64 s[46:47], s[46:47], exec
	s_cselect_b32 s47, s39, s82
	s_cselect_b32 s46, s38, s81
	v_lshl_add_u64 v[200:201], v[190:191], 0, s[44:45]
	s_add_i32 m0, s41, 0x8000
	ds_read_b128 v[220:223], v213
	ds_read_b128 v[228:231], v213 offset:2048
	ds_read_b128 v[224:227], v214
	ds_read_b128 v[232:235], v214 offset:2048
	ds_read_b128 v[236:239], v213 offset:4096
	ds_read_b128 v[244:247], v213 offset:6144
	ds_read_b128 v[240:243], v214 offset:4096
	ds_read_b128 v[248:251], v214 offset:6144
	global_load_lds_dwordx4 v[200:201], off
	v_lshl_add_u64 v[200:201], v[188:189], 0, s[44:45]
	s_add_i32 m0, s41, 0xa000
	s_nop 0
	global_load_lds_dwordx4 v[200:201], off
	v_lshl_add_u64 v[200:201], v[186:187], 0, s[44:45]
	s_add_i32 m0, s41, 0xc000
	s_nop 0
	global_load_lds_dwordx4 v[200:201], off
	v_lshl_add_u64 v[200:201], v[184:185], 0, s[44:45]
	s_add_i32 m0, s41, 0xe000
	s_nop 0
	global_load_lds_dwordx4 v[200:201], off
	s_waitcnt vmcnt(8)
	s_waitcnt lgkmcnt(0)
	s_barrier
	s_setprio 1
	s_waitcnt lgkmcnt(0)
	v_mfma_f32_16x16x128_f8f6f4 v[158:161], v[18:25], v[220:227], 0
	v_mfma_f32_16x16x128_f8f6f4 v[154:157], v[26:33], v[220:227], 0
	v_mfma_f32_16x16x128_f8f6f4 v[150:153], v[18:25], v[228:235], 0
	v_mfma_f32_16x16x128_f8f6f4 v[146:149], v[26:33], v[228:235], 0
	v_mfma_f32_16x16x128_f8f6f4 v[142:145], v[18:25], v[236:243], 0
	v_mfma_f32_16x16x128_f8f6f4 v[138:141], v[26:33], v[236:243], 0
	v_mfma_f32_16x16x128_f8f6f4 v[134:137], v[18:25], v[244:251], 0
	v_mfma_f32_16x16x128_f8f6f4 v[130:133], v[26:33], v[244:251], 0
	s_setprio 0
	s_setprio 1
	v_mfma_f32_16x16x128_f8f6f4 v[102:105], v[2:9], v[220:227], 0
	v_mfma_f32_16x16x128_f8f6f4 v[94:97], v[10:17], v[220:227], 0
	v_mfma_f32_16x16x128_f8f6f4 v[86:89], v[2:9], v[228:235], 0
	v_mfma_f32_16x16x128_f8f6f4 v[82:85], v[10:17], v[228:235], 0
	v_mfma_f32_16x16x128_f8f6f4 v[78:81], v[2:9], v[236:243], 0
	v_mfma_f32_16x16x128_f8f6f4 v[74:77], v[10:17], v[236:243], 0
	v_mfma_f32_16x16x128_f8f6f4 v[70:73], v[2:9], v[244:251], 0
	v_mfma_f32_16x16x128_f8f6f4 v[66:69], v[10:17], v[244:251], 0
	s_setprio 0
	s_barrier
	s_add_i32 s81, s66, s51
	v_lshl_add_u64 v[200:201], s[46:47], 0, v[162:163]
	s_mov_b32 m0, s81
	ds_read_b128 v[220:223], v213 offset:16384
	ds_read_b128 v[228:231], v213 offset:18432
	ds_read_b128 v[224:227], v214 offset:16384
	ds_read_b128 v[232:235], v214 offset:18432
	ds_read_b128 v[236:239], v213 offset:20480
	ds_read_b128 v[244:247], v213 offset:22528
	ds_read_b128 v[240:243], v214 offset:20480
	ds_read_b128 v[248:251], v214 offset:22528
	global_load_lds_dwordx4 v[200:201], off
	s_add_i32 m0, s81, 0x2000
	s_add_u32 s82, s46, 0x40000
	v_lshl_add_u64 v[202:203], s[46:47], 0, v[164:165]
	s_addc_u32 s83, s47, 0
	s_add_i32 s81, s68, s51
	global_load_lds_dwordx4 v[202:203], off
	v_lshl_add_u64 v[252:253], s[82:83], 0, v[162:163]
	s_mov_b32 m0, s81
	s_nop 0
	global_load_lds_dwordx4 v[252:253], off
	v_lshl_add_u64 v[252:253], s[82:83], 0, v[164:165]
	s_add_i32 m0, s81, 0x2000
	s_nop 0
	global_load_lds_dwordx4 v[252:253], off
	s_waitcnt vmcnt(6)
	s_waitcnt lgkmcnt(0)
	s_barrier
	s_setprio 1
	s_waitcnt lgkmcnt(0)
	v_mfma_f32_16x16x128_f8f6f4 v[126:129], v[18:25], v[220:227], 0
	v_mfma_f32_16x16x128_f8f6f4 v[122:125], v[26:33], v[220:227], 0
	v_mfma_f32_16x16x128_f8f6f4 v[118:121], v[18:25], v[228:235], 0
	v_mfma_f32_16x16x128_f8f6f4 v[114:117], v[26:33], v[228:235], 0
	v_mfma_f32_16x16x128_f8f6f4 v[110:113], v[18:25], v[236:243], 0
	v_mfma_f32_16x16x128_f8f6f4 v[106:109], v[26:33], v[236:243], 0
	v_mfma_f32_16x16x128_f8f6f4 v[98:101], v[18:25], v[244:251], 0
	v_mfma_f32_16x16x128_f8f6f4 v[90:93], v[26:33], v[244:251], 0
	s_setprio 0
	s_setprio 1
	v_mfma_f32_16x16x128_f8f6f4 v[62:65], v[2:9], v[220:227], 0
	v_mfma_f32_16x16x128_f8f6f4 v[58:61], v[10:17], v[220:227], 0
	v_mfma_f32_16x16x128_f8f6f4 v[54:57], v[2:9], v[228:235], 0
	v_mfma_f32_16x16x128_f8f6f4 v[50:53], v[10:17], v[228:235], 0
	v_mfma_f32_16x16x128_f8f6f4 v[46:49], v[2:9], v[236:243], 0
	v_mfma_f32_16x16x128_f8f6f4 v[42:45], v[10:17], v[236:243], 0
	v_mfma_f32_16x16x128_f8f6f4 v[38:41], v[2:9], v[244:251], 0
	v_mfma_f32_16x16x128_f8f6f4 v[34:37], v[10:17], v[244:251], 0
	s_setprio 0
	s_barrier
	s_branch .Lp7_blk3

.LBB0_861:
	s_lshl_b32 s37, s79, 8
	s_bitset1_b32 s37, 7
	s_lshl_b32 s35, s79, 19
	v_or_b32_e32 v2, s37, v1
	v_or_b32_e32 v176, s35, v207
	v_lshl_or_b32 v178, v2, 11, v204
	v_or_b32_e32 v180, s35, v208
	v_or_b32_e32 v2, s37, v205
	v_mov_b32_e32 v171, v167
	v_mov_b32_e32 v173, v167
	v_mov_b32_e32 v175, v167
	s_add_u32 s35, s44, 0x100
	v_mov_b32_e32 v34, 0
	v_lshl_or_b32 v182, v2, 11, v206
	v_mov_b32_e32 v177, v167
	v_mov_b32_e32 v181, v167
	v_mov_b32_e32 v179, v167
	v_mov_b32_e32 v183, v167
	v_lshl_add_u64 v[184:185], s[20:21], 0, v[174:175]
	v_lshl_add_u64 v[186:187], s[20:21], 0, v[172:173]
	v_lshl_add_u64 v[188:189], s[20:21], 0, v[170:171]
	v_lshl_add_u64 v[190:191], s[20:21], 0, v[166:167]
	s_addc_u32 s37, s45, 0
	s_mov_b32 s43, -2
	s_mov_b64 s[44:45], 0
	s_andn2_b64 vcc, exec, s[14:15]
	s_cbranch_vccnz .Lp7_entry
	s_barrier

.LBB0_862:
	s_cmp_eq_u32 s44, 0
	s_cbranch_scc1 .Lp7_first
	s_add_u32 s48, s2, s44
	v_add_u32_e32 v2, s66, v210
	s_addc_u32 s49, s3, s45
	v_add_u32_e32 v3, s66, v211
	ds_read_b128 v[18:21], v2
	ds_read_b128 v[22:25], v3
	v_add_u32_e32 v2, s67, v210
	s_add_u32 s81, s48, 0x3e800100
	v_add_u32_e32 v3, s67, v211
	ds_read_b128 v[26:29], v2
	ds_read_b128 v[30:33], v3
	v_add_u32_e32 v2, s68, v210
	v_add_u32_e32 v6, s68, v211
	v_add_u32_e32 v10, s69, v210
	v_add_u32_e32 v14, s69, v211
	s_addc_u32 s82, s49, 0
	ds_read_b128 v[2:5], v2
	ds_read_b128 v[6:9], v6
	ds_read_b128 v[10:13], v10
	ds_read_b128 v[14:17], v14
	s_and_b64 s[48:49], s[46:47], exec
	s_cselect_b32 s49, s9, s82
	s_cselect_b32 s48, s8, s81
	s_add_u32 s81, s35, s44
	s_addc_u32 s82, s37, s45
	s_and_b64 s[46:47], s[46:47], exec
	s_cselect_b32 s47, s39, s82
	s_cselect_b32 s46, s38, s81
	v_lshl_add_u64 v[200:201], v[190:191], 0, s[44:45]
	s_add_i32 m0, s41, 0x8000
	ds_read_b128 v[220:223], v213
	ds_read_b128 v[228:231], v213 offset:2048
	ds_read_b128 v[224:227], v214
	ds_read_b128 v[232:235], v214 offset:2048
	ds_read_b128 v[236:239], v213 offset:4096
	ds_read_b128 v[244:247], v213 offset:6144
	ds_read_b128 v[240:243], v214 offset:4096
	ds_read_b128 v[248:251], v214 offset:6144
	global_load_lds_dwordx4 v[200:201], off
	v_lshl_add_u64 v[200:201], v[188:189], 0, s[44:45]
	s_add_i32 m0, s41, 0xa000
	s_nop 0
	global_load_lds_dwordx4 v[200:201], off
	v_lshl_add_u64 v[200:201], v[186:187], 0, s[44:45]
	s_add_i32 m0, s41, 0xc000
	s_nop 0
	global_load_lds_dwordx4 v[200:201], off
	v_lshl_add_u64 v[200:201], v[184:185], 0, s[44:45]
	s_add_i32 m0, s41, 0xe000
	s_nop 0
	global_load_lds_dwordx4 v[200:201], off
	s_waitcnt vmcnt(8)
	s_waitcnt lgkmcnt(0)
	s_barrier
	s_setprio 1
	s_waitcnt lgkmcnt(0)
	v_mfma_f32_16x16x128_f8f6f4 v[158:161], v[18:25], v[220:227], v[158:161]
	v_mfma_f32_16x16x128_f8f6f4 v[154:157], v[26:33], v[220:227], v[154:157]
	v_mfma_f32_16x16x128_f8f6f4 v[150:153], v[18:25], v[228:235], v[150:153]
	v_mfma_f32_16x16x128_f8f6f4 v[146:149], v[26:33], v[228:235], v[146:149]
	v_mfma_f32_16x16x128_f8f6f4 v[142:145], v[18:25], v[236:243], v[142:145]
	v_mfma_f32_16x16x128_f8f6f4 v[138:141], v[26:33], v[236:243], v[138:141]
	v_mfma_f32_16x16x128_f8f6f4 v[134:137], v[18:25], v[244:251], v[134:137]
	v_mfma_f32_16x16x128_f8f6f4 v[130:133], v[26:33], v[244:251], v[130:133]
	s_setprio 0
	s_setprio 1
	v_mfma_f32_16x16x128_f8f6f4 v[102:105], v[2:9], v[220:227], v[102:105]
	v_mfma_f32_16x16x128_f8f6f4 v[94:97], v[10:17], v[220:227], v[94:97]
	v_mfma_f32_16x16x128_f8f6f4 v[86:89], v[2:9], v[228:235], v[86:89]
	v_mfma_f32_16x16x128_f8f6f4 v[82:85], v[10:17], v[228:235], v[82:85]
	v_mfma_f32_16x16x128_f8f6f4 v[78:81], v[2:9], v[236:243], v[78:81]
	v_mfma_f32_16x16x128_f8f6f4 v[74:77], v[10:17], v[236:243], v[74:77]
	v_mfma_f32_16x16x128_f8f6f4 v[70:73], v[2:9], v[244:251], v[70:73]
	v_mfma_f32_16x16x128_f8f6f4 v[66:69], v[10:17], v[244:251], v[66:69]
	s_setprio 0
	s_barrier
	s_add_i32 s81, s66, s51
	v_lshl_add_u64 v[200:201], s[46:47], 0, v[162:163]
	s_mov_b32 m0, s81
	ds_read_b128 v[220:223], v213 offset:16384
	ds_read_b128 v[228:231], v213 offset:18432
	ds_read_b128 v[224:227], v214 offset:16384
	ds_read_b128 v[232:235], v214 offset:18432
	ds_read_b128 v[236:239], v213 offset:20480
	ds_read_b128 v[244:247], v213 offset:22528
	ds_read_b128 v[240:243], v214 offset:20480
	ds_read_b128 v[248:251], v214 offset:22528
	global_load_lds_dwordx4 v[200:201], off
	s_add_i32 m0, s81, 0x2000
	s_add_u32 s82, s46, 0x40000
	v_lshl_add_u64 v[202:203], s[46:47], 0, v[164:165]
	s_addc_u32 s83, s47, 0
	s_add_i32 s81, s68, s51
	global_load_lds_dwordx4 v[202:203], off
	v_lshl_add_u64 v[252:253], s[82:83], 0, v[162:163]
	s_mov_b32 m0, s81
	s_nop 0
	global_load_lds_dwordx4 v[252:253], off
	v_lshl_add_u64 v[252:253], s[82:83], 0, v[164:165]
	s_add_i32 m0, s81, 0x2000
	s_nop 0
	global_load_lds_dwordx4 v[252:253], off
	s_waitcnt vmcnt(6)
	s_waitcnt lgkmcnt(0)
	s_barrier
	s_setprio 1
	s_waitcnt lgkmcnt(0)
	v_mfma_f32_16x16x128_f8f6f4 v[126:129], v[18:25], v[220:227], v[126:129]
	v_mfma_f32_16x16x128_f8f6f4 v[122:125], v[26:33], v[220:227], v[122:125]
	v_mfma_f32_16x16x128_f8f6f4 v[118:121], v[18:25], v[228:235], v[118:121]
	v_mfma_f32_16x16x128_f8f6f4 v[114:117], v[26:33], v[228:235], v[114:117]
	v_mfma_f32_16x16x128_f8f6f4 v[110:113], v[18:25], v[236:243], v[110:113]
	v_mfma_f32_16x16x128_f8f6f4 v[106:109], v[26:33], v[236:243], v[106:109]
	v_mfma_f32_16x16x128_f8f6f4 v[98:101], v[18:25], v[244:251], v[98:101]
	v_mfma_f32_16x16x128_f8f6f4 v[90:93], v[26:33], v[244:251], v[90:93]
	s_setprio 0
	s_setprio 1
	v_mfma_f32_16x16x128_f8f6f4 v[62:65], v[2:9], v[220:227], v[62:65]
	v_mfma_f32_16x16x128_f8f6f4 v[58:61], v[10:17], v[220:227], v[58:61]
	v_mfma_f32_16x16x128_f8f6f4 v[54:57], v[2:9], v[228:235], v[54:57]
	v_mfma_f32_16x16x128_f8f6f4 v[50:53], v[10:17], v[228:235], v[50:53]
	v_mfma_f32_16x16x128_f8f6f4 v[46:49], v[2:9], v[236:243], v[46:49]
	v_mfma_f32_16x16x128_f8f6f4 v[42:45], v[10:17], v[236:243], v[42:45]
	v_mfma_f32_16x16x128_f8f6f4 v[38:41], v[2:9], v[244:251], v[38:41]
	v_mfma_f32_16x16x128_f8f6f4 v[34:37], v[10:17], v[244:251], v[34:37]
	s_setprio 0
	s_barrier
.Lp7_blk3:
	v_add_u32_e32 v2, s70, v210
	v_add_u32_e32 v6, s70, v211
	v_add_u32_e32 v10, s71, v210
	v_add_u32_e32 v14, s71, v211
	v_add_u32_e32 v18, s72, v210
	v_add_u32_e32 v22, s72, v211
	v_add_u32_e32 v26, s73, v210
	v_add_u32_e32 v30, s73, v211
	ds_read_b128 v[2:5], v2
	ds_read_b128 v[6:9], v6
	ds_read_b128 v[10:13], v10
	ds_read_b128 v[14:17], v14
	ds_read_b128 v[18:21], v18
	ds_read_b128 v[22:25], v22
	ds_read_b128 v[26:29], v26
	ds_read_b128 v[30:33], v30
	s_mov_b32 m0, s41
	v_lshl_add_u64 v[198:199], s[48:49], 0, v[198:199]
	ds_read_b128 v[220:223], v213 offset:32768
	ds_read_b128 v[228:231], v213 offset:34816
	ds_read_b128 v[224:227], v214 offset:32768
	ds_read_b128 v[232:235], v214 offset:34816
	ds_read_b128 v[236:239], v213 offset:36864
	ds_read_b128 v[244:247], v213 offset:38912
	ds_read_b128 v[240:243], v214 offset:36864
	ds_read_b128 v[248:251], v214 offset:38912
	global_load_lds_dwordx4 v[198:199], off
	v_lshl_add_u64 v[196:197], s[48:49], 0, v[196:197]
	s_mov_b32 m0, s53
	v_lshl_add_u64 v[194:195], s[48:49], 0, v[194:195]
	global_load_lds_dwordx4 v[196:197], off
	s_mov_b32 m0, s54
	v_lshl_add_u64 v[192:193], s[48:49], 0, v[192:193]
	global_load_lds_dwordx4 v[194:195], off
	s_mov_b32 m0, s55
	s_nop 0
	global_load_lds_dwordx4 v[192:193], off
	s_waitcnt vmcnt(8)
	s_waitcnt lgkmcnt(0)
	s_barrier
	s_setprio 1
	s_waitcnt lgkmcnt(0)
	v_mfma_f32_16x16x128_f8f6f4 v[158:161], v[2:9], v[220:227], v[158:161]
	v_mfma_f32_16x16x128_f8f6f4 v[154:157], v[10:17], v[220:227], v[154:157]
	v_mfma_f32_16x16x128_f8f6f4 v[150:153], v[2:9], v[228:235], v[150:153]
	v_mfma_f32_16x16x128_f8f6f4 v[146:149], v[10:17], v[228:235], v[146:149]
	v_mfma_f32_16x16x128_f8f6f4 v[142:145], v[2:9], v[236:243], v[142:145]
	v_mfma_f32_16x16x128_f8f6f4 v[138:141], v[10:17], v[236:243], v[138:141]
	v_mfma_f32_16x16x128_f8f6f4 v[134:137], v[2:9], v[244:251], v[134:137]
	v_mfma_f32_16x16x128_f8f6f4 v[130:133], v[10:17], v[244:251], v[130:133]
	s_setprio 0
	s_setprio 1
	v_mfma_f32_16x16x128_f8f6f4 v[102:105], v[18:25], v[220:227], v[102:105]
	v_mfma_f32_16x16x128_f8f6f4 v[94:97], v[26:33], v[220:227], v[94:97]
	v_mfma_f32_16x16x128_f8f6f4 v[86:89], v[18:25], v[228:235], v[86:89]
	v_mfma_f32_16x16x128_f8f6f4 v[82:85], v[26:33], v[228:235], v[82:85]
	v_mfma_f32_16x16x128_f8f6f4 v[78:81], v[18:25], v[236:243], v[78:81]
	v_mfma_f32_16x16x128_f8f6f4 v[74:77], v[26:33], v[236:243], v[74:77]
	v_mfma_f32_16x16x128_f8f6f4 v[70:73], v[18:25], v[244:251], v[70:73]
	v_mfma_f32_16x16x128_f8f6f4 v[66:69], v[26:33], v[244:251], v[66:69]
	s_setprio 0
	s_barrier
	s_add_i32 s48, s70, s51
	v_lshl_add_u64 v[200:201], v[200:201], 0, s[10:11]
	s_mov_b32 m0, s48
	ds_read_b128 v[192:195], v213 offset:49152
	ds_read_b128 v[220:223], v213 offset:51200
	ds_read_b128 v[196:199], v214 offset:49152
	ds_read_b128 v[224:227], v214 offset:51200
	ds_read_b128 v[228:231], v213 offset:53248
	ds_read_b128 v[236:239], v213 offset:55296
	ds_read_b128 v[232:235], v214 offset:53248
	ds_read_b128 v[240:243], v214 offset:55296
	global_load_lds_dwordx4 v[200:201], off
	s_add_i32 m0, s48, 0x2000
	s_add_u32 s46, s46, 0x40080
	v_lshl_add_u64 v[200:201], v[202:203], 0, s[10:11]
	s_addc_u32 s47, s47, 0
	s_add_i32 s48, s72, s51
	global_load_lds_dwordx4 v[200:201], off
	v_lshl_add_u64 v[200:201], s[46:47], 0, v[162:163]
	s_mov_b32 m0, s48
	s_nop 0
	global_load_lds_dwordx4 v[200:201], off
	v_lshl_add_u64 v[200:201], s[46:47], 0, v[164:165]
	s_add_i32 m0, s48, 0x2000
	s_nop 0
	global_load_lds_dwordx4 v[200:201], off
	s_waitcnt vmcnt(6)
	s_waitcnt lgkmcnt(0)
	s_barrier
	s_setprio 1
	s_waitcnt lgkmcnt(0)
	v_mfma_f32_16x16x128_f8f6f4 v[126:129], v[2:9], v[192:199], v[126:129]
	v_mfma_f32_16x16x128_f8f6f4 v[122:125], v[10:17], v[192:199], v[122:125]
	v_mfma_f32_16x16x128_f8f6f4 v[118:121], v[2:9], v[220:227], v[118:121]
	v_mfma_f32_16x16x128_f8f6f4 v[114:117], v[10:17], v[220:227], v[114:117]
	v_mfma_f32_16x16x128_f8f6f4 v[110:113], v[2:9], v[228:235], v[110:113]
	v_mfma_f32_16x16x128_f8f6f4 v[106:109], v[10:17], v[228:235], v[106:109]
	v_mfma_f32_16x16x128_f8f6f4 v[98:101], v[2:9], v[236:243], v[98:101]
	v_mfma_f32_16x16x128_f8f6f4 v[90:93], v[10:17], v[236:243], v[90:93]
	s_setprio 0
	s_setprio 1
	v_mfma_f32_16x16x128_f8f6f4 v[62:65], v[18:25], v[192:199], v[62:65]
	v_mfma_f32_16x16x128_f8f6f4 v[58:61], v[26:33], v[192:199], v[58:61]
	v_mfma_f32_16x16x128_f8f6f4 v[54:57], v[18:25], v[220:227], v[54:57]
	v_mfma_f32_16x16x128_f8f6f4 v[50:53], v[26:33], v[220:227], v[50:53]
	v_mfma_f32_16x16x128_f8f6f4 v[46:49], v[18:25], v[228:235], v[46:49]
	v_mfma_f32_16x16x128_f8f6f4 v[42:45], v[26:33], v[228:235], v[42:45]
	v_mfma_f32_16x16x128_f8f6f4 v[38:41], v[18:25], v[236:243], v[38:41]
	v_mfma_f32_16x16x128_f8f6f4 v[34:37], v[26:33], v[236:243], v[34:37]
	s_setprio 0
	s_barrier
	s_add_i32 s43, s43, 2
	s_add_u32 s44, s44, 0x100
	s_addc_u32 s45, s45, 0
	s_cmp_gt_u32 s43, 13
	s_cbranch_scc1 .LBB0_866
